# T10 variant: 8192 items moved, waves 1..4, one half-item unit per wave per seam, no store-ack wait before the closing barrier
# speedup vs baseline: 1.0072x; 1.0028x over previous
; __device__ __forceinline__ void transpose_item_f8(const float* W, int N, unsigned char* WT, int ldt, int kind, int off, int item, int lane, float scale) {
;     const int nblk = N >> 6, kb = item / nblk, nb = item - kb * nblk, k0 = 128 * kb + 16 * (lane & 7), n = 64 * nb + 4 * (lane >> 3);
;     const f32x4* src = (const f32x4*)(W + (size_t)k0 * N + n);
;     f32x4 v[2][16];
; #pragma unroll
;     for (int hh = 0; hh < 2; ++hh)
; #pragma unroll
;         for (int j = 0; j < 16; ++j) v[hh][j] = __builtin_nontemporal_load(src + (size_t)j * (N >> 2) + 8 * hh);
; #pragma unroll
;     for (int hh = 0; hh < 2; ++hh)
; #pragma unroll
;         for (int i = 0; i < 4; ++i) { v4u o; o.x = pg8::pk4_fp8(v[hh][0][i] * scale, v[hh][1][i] * scale, v[hh][2][i] * scale, v[hh][3][i] * scale); o.y = pg8::pk4_fp8(v[hh][4][i] * scale, v[hh][5][i] * scale, v[hh][6][i] * scale, v[hh][7][i] * scale);
;             o.z = pg8::pk4_fp8(v[hh][8][i] * scale, v[hh][9][i] * scale, v[hh][10][i] * scale, v[hh][11][i] * scale); o.w = pg8::pk4_fp8(v[hh][12][i] * scale, v[hh][13][i] * scale, v[hh][14][i] * scale, v[hh][15][i] * scale);
;             __builtin_nontemporal_store(o, (v4u*)(WT + (size_t)rowmap(kind, off, n + 32 * hh + i) * ldt + k0)); }
; __device__ __forceinline__ void moe_convert(Frame& F, int lo, int hi, int rank, int nrank) {
;     ...
;     for (int it = lo + rank; it < hi; it += nrank) {
;         int r = it; const float* W; unsigned char* WT; int N, ldt, kind, off; float f8s;
;         if (r < 14336) { const int e = r / 1792; r -= e * 1792; W = F.in[IN_WMG] + (size_t)e * 2048 * DFFE; N = DFFE; WT = F.ws + WS_WGU1 + (size_t)e * 14336 * 2048; ldt = 2048; kind = 1; off = 0; f8s = 32.f; }
;         else if ((r -= 14336) < 14336) { const int e = r / 1792; r -= e * 1792; W = F.in[IN_WMU] + (size_t)e * 2048 * DFFE; N = DFFE; WT = F.ws + WS_WGU1 + (size_t)e * 14336 * 2048; ldt = 2048; kind = 1; off = 128; f8s = 256.f; }
;         else { r -= 14336; const int e = r / 1792; r -= e * 1792; W = F.in[IN_WMD] + (size_t)e * DFFE * 2048; N = 2048; WT = F.ws + WS_WDN1 + (size_t)e * 2048 * DFFE; ldt = DFFE; kind = 0; off = 0; f8s = 64.f; }
;         transpose_item_f8(W, N, WT, ldt, kind, off, r, F.lane, f8s);
.LBB0_235:
	s_cmp_gt_i32 s24, 0x67ff
	s_cbranch_scc1 .LBB0_246
	s_add_u32 s14, s86, 0x23800000
	s_addc_u32 s15, s87, 0
	v_lshlrev_b32_e32 v1, 4, v0
	s_waitcnt vmcnt(2)
	v_lshrrev_b32_e32 v2, 1, v0
	s_add_u32 s16, s86, 0x7800000
	v_and_b32_e32 v1, 0x70, v1
	v_and_b32_e32 v134, 28, v2
	s_addc_u32 s17, s87, 0
	s_add_i32 s18, s24, 0xffff9000
	s_mov_b32 s3, 0
	s_mov_b32 s19, 0xc3e00000
	v_mov_b32_e32 v135, 0x43e00000
	v_mov_b32_e32 v136, 0x5c
	s_movk_i32 s20, 0x5d
	s_movk_i32 s21, 0x5e
	s_movk_i32 s22, 0x5f
	s_movk_i32 s23, 0x7c
	s_movk_i32 s26, 0x7d
	s_movk_i32 s27, 0x7e
	s_movk_i32 s28, 0x7f
	s_mov_b32 s29, s24
	s_branch .LBB0_238
.LBB0_237:
	s_lshr_b32 s12, s2, 6
	v_cvt_f32_u32_e32 v2, s12
	s_sub_i32 s35, 0, s12
	s_abs_i32 s34, s33
	s_ashr_i32 s13, s33, 31
	v_rcp_iflag_f32_e32 v2, v2
	v_mov_b32_e32 v138, 0
	v_mov_b32_e32 v139, 0
	v_mov_b32_e32 v140, 0
	v_mul_f32_e32 v2, 0x4f7ffffe, v2
	v_cvt_u32_f32_e32 v2, v2
	v_mov_b32_e32 v141, 0
	v_readfirstlane_b32 s36, v2
	s_mul_i32 s35, s35, s36
	s_mul_hi_u32 s35, s36, s35
	s_add_i32 s36, s36, s35
	s_mul_hi_u32 s35, s34, s36
	s_mul_i32 s36, s35, s12
	s_sub_i32 s34, s34, s36
	s_add_i32 s37, s35, 1
	s_sub_i32 s36, s34, s12
	s_cmp_ge_u32 s34, s12
	s_cselect_b32 s35, s37, s35
	s_cselect_b32 s34, s36, s34
	s_add_i32 s36, s35, 1
	s_cmp_ge_u32 s34, s12
	s_cselect_b32 s34, s36, s35
	s_xor_b32 s34, s34, s13
	s_sub_i32 s13, s34, s13
	v_lshl_or_b32 v132, s13, 7, v1
	s_mul_i32 s12, s13, s12
	v_mad_u64_u32 v[2:3], s[34:35], v132, s2, 0
	s_sub_i32 s12, s33, s12
	v_ashrrev_i32_e32 v133, 31, v132
	v_mov_b32_e32 v4, v3
	s_lshl_b32 s13, s12, 6
	v_mad_u64_u32 v[4:5], s[34:35], v133, s2, v[4:5]
	v_or_b32_e32 v130, s13, v134
	v_mov_b32_e32 v3, v4
	v_lshl_add_u64 v[2:3], v[2:3], 2, s[10:11]
	v_ashrrev_i32_e32 v131, 31, v130
	v_lshl_add_u64 v[2:3], v[130:131], 2, v[2:3]
	s_lshr_b32 s10, s2, 2
	s_mov_b32 s11, s3
	v_lshl_add_u64 v[4:5], s[10:11], 4, v[2:3]
	s_lshr_b32 s34, s2, 1
	s_mov_b32 s35, s3
	global_load_dwordx4 v[66:69], v[2:3], off nt
	global_load_dwordx4 v[70:73], v[4:5], off nt
	s_waitcnt vmcnt(2)
	v_lshl_add_u64 v[6:7], s[34:35], 4, v[2:3]
	s_mul_i32 s34, s10, 3
	s_mul_i32 s36, s10, 6
	s_mov_b32 s37, s3
	v_lshl_add_u64 v[8:9], s[34:35], 4, v[2:3]
	s_ashr_i32 s35, s2, 31
	s_mov_b32 s34, s2
	v_lshl_add_u64 v[12:13], s[36:37], 4, v[2:3]
	s_mul_i32 s36, s10, 7
	v_lshl_add_u64 v[10:11], s[2:3], 4, v[2:3]
	v_lshl_add_u64 v[14:15], s[36:37], 4, v[2:3]
	v_lshl_add_u64 v[16:17], s[34:35], 4, v[4:5]
	global_load_dwordx4 v[74:77], v[10:11], off nt
	global_load_dwordx4 v[90:93], v[12:13], off nt
	global_load_dwordx4 v[86:89], v[14:15], off nt
	global_load_dwordx4 v[102:105], v[16:17], off nt
	s_lshl_b32 s2, s2, 1
	global_load_dwordx4 v[82:85], v[6:7], off nt
	global_load_dwordx4 v[78:81], v[8:9], off nt
	v_lshl_add_u64 v[18:19], s[2:3], 4, v[2:3]
	s_mul_i32 s2, s10, 9
	v_lshl_add_u64 v[20:21], s[2:3], 4, v[2:3]
	global_load_dwordx4 v[94:97], v[18:19], off nt
	global_load_dwordx4 v[98:101], v[20:21], off nt
	s_mul_i32 s2, s10, 10
	v_lshl_add_u64 v[54:55], s[2:3], 4, v[2:3]
	s_mul_i32 s2, s10, 11
	v_lshl_add_u64 v[56:57], s[2:3], 4, v[2:3]
	s_mul_i32 s2, s10, 12
	global_load_dwordx4 v[114:117], v[54:55], off nt
	global_load_dwordx4 v[106:109], v[56:57], off nt
	v_lshl_add_u64 v[58:59], s[2:3], 4, v[2:3]
	s_mul_i32 s2, s10, 13
	v_lshl_add_u64 v[60:61], s[2:3], 4, v[2:3]
	global_load_dwordx4 v[110:113], v[58:59], off nt
	global_load_dwordx4 v[118:121], v[60:61], off nt
	s_mul_i32 s2, s10, 14
	v_lshl_add_u64 v[62:63], s[2:3], 4, v[2:3]
	s_mul_i32 s2, s10, 15
	v_lshl_add_u64 v[142:143], s[2:3], 4, v[2:3]
	global_load_dwordx4 v[122:125], v[62:63], off nt
	global_load_dwordx4 v[126:129], v[142:143], off nt
	global_load_dwordx4 v[42:45], v[2:3], off offset:128 nt
	global_load_dwordx4 v[46:49], v[4:5], off offset:128 nt
	global_load_dwordx4 v[50:53], v[6:7], off offset:128 nt
	global_load_dwordx4 v[38:41], v[8:9], off offset:128 nt
	global_load_dwordx4 v[30:33], v[10:11], off offset:128 nt
	global_load_dwordx4 v[26:29], v[12:13], off offset:128 nt
	global_load_dwordx4 v[22:25], v[14:15], off offset:128 nt
	global_load_dwordx4 v[34:37], v[16:17], off offset:128 nt
	s_nop 0
	global_load_dwordx4 v[10:13], v[18:19], off offset:128 nt
	global_load_dwordx4 v[14:17], v[20:21], off offset:128 nt
	s_nop 0
	global_load_dwordx4 v[18:21], v[54:55], off offset:128 nt
	global_load_dwordx4 v[6:9], v[56:57], off offset:128 nt
	global_load_dwordx4 v[2:5], v[58:59], off offset:128 nt
	s_lshl_b32 s2, s12, 7
	s_and_b32 s2, s2, 0xffffff00
	s_or_b32 s2, s2, s30
	v_lshl_add_u64 v[132:133], s[8:9], 0, v[132:133]
	s_add_i32 s29, s29, s25
	s_add_i32 s18, s18, s25
	s_cmp_lt_i32 s29, 0x6800
	s_waitcnt vmcnt(28)
	v_mul_f32_e32 v54, s31, v66
	s_waitcnt vmcnt(27)
	v_mul_f32_e32 v55, s31, v70
	v_med3_f32 v54, v54, s19, v135
	v_med3_f32 v55, v55, s19, v135
	v_cvt_pk_fp8_f32 v138, v54, v55
	s_waitcnt vmcnt(26)
	v_mul_f32_e32 v58, s31, v74
	v_med3_f32 v58, v58, s19, v135
	s_waitcnt vmcnt(25)
	v_mul_f32_e32 v59, s31, v90
	s_waitcnt vmcnt(23)
	v_mul_f32_e32 v65, s31, v102
	v_med3_f32 v54, v65, s19, v135
	s_waitcnt vmcnt(22)
	v_mul_f32_e32 v56, s31, v82
	s_waitcnt vmcnt(21)
	v_mul_f32_e32 v57, s31, v78
	v_cvt_pk_fp8_f32 v139, v58, v54
	v_med3_f32 v54, v56, s19, v135
	v_med3_f32 v55, v57, s19, v135
	v_cvt_pk_fp8_f32 v138, v54, v55 op_sel:[0,0,1]
	s_waitcnt vmcnt(20)
	v_mul_f32_e32 v54, s31, v94
	s_waitcnt vmcnt(19)
	v_mul_f32_e32 v55, s31, v98
	v_med3_f32 v54, v54, s19, v135
	v_med3_f32 v55, v55, s19, v135
	v_mul_f32_e32 v64, s31, v86
	v_cvt_pk_fp8_f32 v140, v54, v55
	v_med3_f32 v56, v59, s19, v135
	v_med3_f32 v57, v64, s19, v135
	v_cvt_pk_fp8_f32 v139, v56, v57 op_sel:[0,0,1]
	s_waitcnt vmcnt(18)
; __device__ __forceinline__ unsigned pk4_fp8(float a, float b, float c, float d) { int w = 0; w = __builtin_amdgcn_cvt_pk_fp8_f32(clamp448(a), clamp448(b), w, false); w = __builtin_amdgcn_cvt_pk_fp8_f32(clamp448(c), clamp448(d), w, true); return (unsigned)w; }
; __device__ __forceinline__ int rowmap(int kind, int off, int n) {
;     if (kind == 0) return off + n;
;     if (kind == 1) return off + ((n >> 7) << 8) + (n & 127);
;     if (n < 1536) return n; if (n < 1544) return 4352 + (n - 1536); if (n < 3080) return n - 8; if (n < 3096) return 4360 + (n - 3080); return n - 24;
; __device__ __forceinline__ void transpose_item_f8(const float* W, int N, unsigned char* WT, int ldt, int kind, int off, int item, int lane, float scale) {
;     ...
; #pragma unroll
;     for (int hh = 0; hh < 2; ++hh)
; #pragma unroll
;         for (int i = 0; i < 4; ++i) { v4u o; o.x = pg8::pk4_fp8(v[hh][0][i] * scale, v[hh][1][i] * scale, v[hh][2][i] * scale, v[hh][3][i] * scale); o.y = pg8::pk4_fp8(v[hh][4][i] * scale, v[hh][5][i] * scale, v[hh][6][i] * scale, v[hh][7][i] * scale);
;             o.z = pg8::pk4_fp8(v[hh][8][i] * scale, v[hh][9][i] * scale, v[hh][10][i] * scale, v[hh][11][i] * scale); o.w = pg8::pk4_fp8(v[hh][12][i] * scale, v[hh][13][i] * scale, v[hh][14][i] * scale, v[hh][15][i] * scale);
;             __builtin_nontemporal_store(o, (v4u*)(WT + (size_t)rowmap(kind, off, n + 32 * hh + i) * ldt + k0)); }
	v_mul_f32_e32 v56, s31, v114
	s_waitcnt vmcnt(17)
	v_mul_f32_e32 v54, s31, v106
	v_med3_f32 v55, v56, s19, v135
	v_med3_f32 v54, v54, s19, v135
	v_cvt_pk_fp8_f32 v140, v55, v54 op_sel:[0,0,1]
	s_waitcnt vmcnt(16)
	v_mul_f32_e32 v54, s31, v110
	s_waitcnt vmcnt(15)
	v_mul_f32_e32 v59, s31, v118
	v_med3_f32 v58, v54, s19, v135
	v_med3_f32 v59, v59, s19, v135
	v_cvt_pk_fp8_f32 v141, v58, v59
	s_waitcnt vmcnt(14)
	v_mul_f32_e32 v58, s31, v122
	s_waitcnt vmcnt(13)
	v_mul_f32_e32 v70, s31, v126
	v_med3_f32 v66, v58, s19, v135
	v_med3_f32 v70, v70, s19, v135
	v_cvt_pk_fp8_f32 v141, v66, v70 op_sel:[0,0,1]
	v_bitop3_b32 v66, s13, v136, v134 bitop3:0xc8
	v_or_b32_e32 v66, s2, v66
	v_add_u32_e32 v70, s30, v130
	v_cndmask_b32_e64 v66, v66, v70, s[4:5]
	v_ashrrev_i32_e32 v70, 31, v66
	global_load_dwordx4 v[54:57], v[60:61], off offset:128 nt
	v_mul_lo_u32 v70, s6, v70
	global_load_dwordx4 v[62:65], v[62:63], off offset:128 nt
	v_mul_lo_u32 v74, s7, v66
	global_load_dwordx4 v[58:61], v[142:143], off offset:128 nt
	v_mad_u64_u32 v[142:143], s[8:9], s6, v66, v[132:133]
	v_add3_u32 v143, v74, v143, v70
	v_mul_f32_e32 v66, s31, v67
	v_mul_f32_e32 v67, s31, v71
	global_store_dwordx4 v[142:143], v[138:141], off nt
	v_med3_f32 v66, v66, s19, v135
	v_med3_f32 v67, v67, s19, v135
	v_mov_b32_e32 v138, 0
	v_cvt_pk_fp8_f32 v138, v66, v67
	v_mul_f32_e32 v66, s31, v83
	v_mul_f32_e32 v67, s31, v79
	v_med3_f32 v66, v66, s19, v135
	v_med3_f32 v67, v67, s19, v135
	v_cvt_pk_fp8_f32 v138, v66, v67 op_sel:[0,0,1]
	v_mul_f32_e32 v66, s31, v75
	v_mul_f32_e32 v67, s31, v103
	v_med3_f32 v66, v66, s19, v135
	v_med3_f32 v67, v67, s19, v135
	v_mov_b32_e32 v139, 0
	v_cvt_pk_fp8_f32 v139, v66, v67
	v_mul_f32_e32 v66, s31, v91
	v_mul_f32_e32 v67, s31, v87
	v_med3_f32 v66, v66, s19, v135
	v_med3_f32 v67, v67, s19, v135
	v_cvt_pk_fp8_f32 v139, v66, v67 op_sel:[0,0,1]
	v_mul_f32_e32 v66, s31, v95
	v_mul_f32_e32 v67, s31, v99
	v_med3_f32 v66, v66, s19, v135
	v_med3_f32 v67, v67, s19, v135
	v_mov_b32_e32 v140, 0
	v_cvt_pk_fp8_f32 v140, v66, v67
	v_mul_f32_e32 v66, s31, v115
	v_mul_f32_e32 v67, s31, v107
	v_med3_f32 v66, v66, s19, v135
	v_med3_f32 v67, v67, s19, v135
	v_cvt_pk_fp8_f32 v140, v66, v67 op_sel:[0,0,1]
	v_mul_f32_e32 v66, s31, v111
	v_mul_f32_e32 v67, s31, v119
	v_med3_f32 v66, v66, s19, v135
	v_med3_f32 v67, v67, s19, v135
	v_mov_b32_e32 v141, 0
	v_cvt_pk_fp8_f32 v141, v66, v67
	v_mul_f32_e32 v66, s31, v123
	v_mul_f32_e32 v67, s31, v127
	v_med3_f32 v66, v66, s19, v135
	v_med3_f32 v67, v67, s19, v135
	v_cvt_pk_fp8_f32 v141, v66, v67 op_sel:[0,0,1]
	v_or_b32_e32 v66, 1, v130
	v_bitop3_b32 v67, v130, s20, 1 bitop3:0xc8
	v_add_u32_e32 v66, s30, v66
	v_or_b32_e32 v67, s2, v67
	v_cndmask_b32_e64 v66, v67, v66, s[4:5]
	v_ashrrev_i32_e32 v67, 31, v66
	v_mul_lo_u32 v70, s6, v67
	v_mul_lo_u32 v71, s7, v66
	v_mad_u64_u32 v[66:67], s[8:9], s6, v66, v[132:133]
	v_add3_u32 v67, v71, v67, v70
	global_store_dwordx4 v[66:67], v[138:141], off nt
	v_mul_f32_e32 v66, s31, v68
	v_mul_f32_e32 v67, s31, v72
	v_med3_f32 v66, v66, s19, v135
	v_med3_f32 v67, v67, s19, v135
	v_mov_b32_e32 v138, 0
	v_cvt_pk_fp8_f32 v138, v66, v67
	v_mul_f32_e32 v66, s31, v84
	v_mul_f32_e32 v67, s31, v80
	v_med3_f32 v66, v66, s19, v135
	v_med3_f32 v67, v67, s19, v135
	v_cvt_pk_fp8_f32 v138, v66, v67 op_sel:[0,0,1]
	v_mul_f32_e32 v66, s31, v76
	v_mul_f32_e32 v67, s31, v104
	v_med3_f32 v66, v66, s19, v135
	v_med3_f32 v67, v67, s19, v135
	v_mov_b32_e32 v139, 0
	v_cvt_pk_fp8_f32 v139, v66, v67
	v_mul_f32_e32 v66, s31, v92
	v_mul_f32_e32 v67, s31, v88
	v_med3_f32 v66, v66, s19, v135
	v_med3_f32 v67, v67, s19, v135
	v_cvt_pk_fp8_f32 v139, v66, v67 op_sel:[0,0,1]
	v_mul_f32_e32 v66, s31, v96
	v_mul_f32_e32 v67, s31, v100
	v_med3_f32 v66, v66, s19, v135
	v_med3_f32 v67, v67, s19, v135
	v_mov_b32_e32 v140, 0
	v_cvt_pk_fp8_f32 v140, v66, v67
	v_mul_f32_e32 v66, s31, v116
	v_mul_f32_e32 v67, s31, v108
	v_med3_f32 v66, v66, s19, v135
	v_med3_f32 v67, v67, s19, v135
	v_cvt_pk_fp8_f32 v140, v66, v67 op_sel:[0,0,1]
	v_mul_f32_e32 v66, s31, v112
	v_mul_f32_e32 v67, s31, v120
	v_med3_f32 v66, v66, s19, v135
	v_med3_f32 v67, v67, s19, v135
	v_mov_b32_e32 v141, 0
	v_cvt_pk_fp8_f32 v141, v66, v67
	v_mul_f32_e32 v66, s31, v124
	v_mul_f32_e32 v67, s31, v128
	v_med3_f32 v66, v66, s19, v135
	v_med3_f32 v67, v67, s19, v135
	v_cvt_pk_fp8_f32 v141, v66, v67 op_sel:[0,0,1]
	v_or_b32_e32 v66, 2, v130
	v_bitop3_b32 v67, v130, s21, 2 bitop3:0xc8
	v_add_u32_e32 v66, s30, v66
	v_or_b32_e32 v67, s2, v67
	v_cndmask_b32_e64 v66, v67, v66, s[4:5]
	v_ashrrev_i32_e32 v67, 31, v66
	v_mul_lo_u32 v68, s6, v67
	v_mul_lo_u32 v70, s7, v66
	v_mad_u64_u32 v[66:67], s[8:9], s6, v66, v[132:133]
	v_add3_u32 v67, v70, v67, v68
	global_store_dwordx4 v[66:67], v[138:141], off nt
	v_mul_f32_e32 v66, s31, v69
	v_mul_f32_e32 v67, s31, v73
	v_med3_f32 v69, v66, s19, v135
	v_med3_f32 v67, v67, s19, v135
	v_mov_b32_e32 v66, 0
	v_cvt_pk_fp8_f32 v66, v69, v67
	v_mul_f32_e32 v68, s31, v85
	v_mul_f32_e32 v67, s31, v81
	v_med3_f32 v68, v68, s19, v135
	v_med3_f32 v67, v67, s19, v135
	v_cvt_pk_fp8_f32 v66, v68, v67 op_sel:[0,0,1]
	v_mul_f32_e32 v67, s31, v77
	v_mul_f32_e32 v68, s31, v105
	v_med3_f32 v70, v67, s19, v135
	v_med3_f32 v68, v68, s19, v135
	v_mov_b32_e32 v67, 0
	v_cvt_pk_fp8_f32 v67, v70, v68
	v_mul_f32_e32 v69, s31, v93
	v_mul_f32_e32 v68, s31, v89
	v_med3_f32 v69, v69, s19, v135
	v_med3_f32 v68, v68, s19, v135
	v_cvt_pk_fp8_f32 v67, v69, v68 op_sel:[0,0,1]
	v_mul_f32_e32 v68, s31, v97
	v_mul_f32_e32 v69, s31, v101
	v_med3_f32 v71, v68, s19, v135
	v_med3_f32 v69, v69, s19, v135
	v_mov_b32_e32 v68, 0
	v_cvt_pk_fp8_f32 v68, v71, v69
	v_mul_f32_e32 v70, s31, v117
	v_mul_f32_e32 v69, s31, v109
	v_med3_f32 v70, v70, s19, v135
	v_med3_f32 v69, v69, s19, v135
	v_cvt_pk_fp8_f32 v68, v70, v69 op_sel:[0,0,1]
	v_mul_f32_e32 v69, s31, v113
	v_mul_f32_e32 v70, s31, v121
	v_med3_f32 v72, v69, s19, v135
	v_med3_f32 v70, v70, s19, v135
	v_mov_b32_e32 v69, 0
	v_cvt_pk_fp8_f32 v69, v72, v70
	v_mul_f32_e32 v71, s31, v125
	v_mul_f32_e32 v70, s31, v129
	v_med3_f32 v71, v71, s19, v135
	v_med3_f32 v70, v70, s19, v135
	v_cvt_pk_fp8_f32 v69, v71, v70 op_sel:[0,0,1]
	v_or_b32_e32 v70, 3, v130
	v_bitop3_b32 v71, v130, s22, 3 bitop3:0xc8
	v_add_u32_e32 v70, s30, v70
	v_or_b32_e32 v71, s2, v71
	v_cndmask_b32_e64 v72, v71, v70, s[4:5]
	v_ashrrev_i32_e32 v70, 31, v72
	v_mul_lo_u32 v73, s6, v70
	v_mad_u64_u32 v[70:71], s[8:9], s6, v72, v[132:133]
	v_mul_lo_u32 v72, s7, v72
	v_add3_u32 v71, v72, v71, v73
	s_waitcnt vmcnt(10)
; __device__ __forceinline__ unsigned pk4_fp8(float a, float b, float c, float d) { int w = 0; w = __builtin_amdgcn_cvt_pk_fp8_f32(clamp448(a), clamp448(b), w, false); w = __builtin_amdgcn_cvt_pk_fp8_f32(clamp448(c), clamp448(d), w, true); return (unsigned)w; }
; __device__ __forceinline__ void transpose_item_f8(const float* W, int N, unsigned char* WT, int ldt, int kind, int off, int item, int lane, float scale) {
;     ...
; #pragma unroll
;     for (int hh = 0; hh < 2; ++hh)
; #pragma unroll
;         for (int i = 0; i < 4; ++i) { v4u o; o.x = pg8::pk4_fp8(v[hh][0][i] * scale, v[hh][1][i] * scale, v[hh][2][i] * scale, v[hh][3][i] * scale); o.y = pg8::pk4_fp8(v[hh][4][i] * scale, v[hh][5][i] * scale, v[hh][6][i] * scale, v[hh][7][i] * scale);
;             o.z = pg8::pk4_fp8(v[hh][8][i] * scale, v[hh][9][i] * scale, v[hh][10][i] * scale, v[hh][11][i] * scale); o.w = pg8::pk4_fp8(v[hh][12][i] * scale, v[hh][13][i] * scale, v[hh][14][i] * scale, v[hh][15][i] * scale);
;             __builtin_nontemporal_store(o, (v4u*)(WT + (size_t)rowmap(kind, off, n + 32 * hh + i) * ldt + k0)); }
	v_mul_f32_e32 v10, s31, v10
	s_waitcnt vmcnt(9)
	v_mul_f32_e32 v14, s31, v14
	global_store_dwordx4 v[70:71], v[66:69], off nt
	v_med3_f32 v10, v10, s19, v135
	v_med3_f32 v14, v14, s19, v135
	v_mov_b32_e32 v68, 0
	v_cvt_pk_fp8_f32 v68, v10, v14
	s_waitcnt vmcnt(9)
	v_mul_f32_e32 v18, s31, v18
	s_waitcnt vmcnt(8)
	v_mul_f32_e32 v6, s31, v6
	v_med3_f32 v10, v18, s19, v135
	v_med3_f32 v6, v6, s19, v135
	v_cvt_pk_fp8_f32 v68, v10, v6 op_sel:[0,0,1]
	s_waitcnt vmcnt(7)
	v_mul_f32_e32 v2, s31, v2
	s_waitcnt vmcnt(6)
	v_mul_f32_e32 v6, s31, v54
	v_med3_f32 v2, v2, s19, v135
	v_med3_f32 v6, v6, s19, v135
	v_mov_b32_e32 v69, 0
	v_mul_f32_e32 v42, s31, v42
	v_mul_f32_e32 v46, s31, v46
	v_mul_f32_e32 v30, s31, v30
	v_mul_f32_e32 v34, s31, v34
	v_cvt_pk_fp8_f32 v69, v2, v6
	v_med3_f32 v42, v42, s19, v135
	v_med3_f32 v46, v46, s19, v135
	v_mov_b32_e32 v66, 0
	v_med3_f32 v30, v30, s19, v135
	v_med3_f32 v34, v34, s19, v135
	v_mov_b32_e32 v67, 0
	v_cvt_pk_fp8_f32 v66, v42, v46
	v_cvt_pk_fp8_f32 v67, v30, v34
	s_waitcnt vmcnt(5)
	v_mul_f32_e32 v10, s31, v62
	s_waitcnt vmcnt(4)
	v_mul_f32_e32 v2, s31, v58
	v_med3_f32 v6, v10, s19, v135
	v_med3_f32 v2, v2, s19, v135
	v_or_b32_e32 v70, 32, v130
	v_mul_f32_e32 v50, s31, v50
	v_mul_f32_e32 v38, s31, v38
	v_mul_f32_e32 v26, s31, v26
	v_mul_f32_e32 v22, s31, v22
	v_cvt_pk_fp8_f32 v69, v6, v2 op_sel:[0,0,1]
	v_bitop3_b32 v6, v130, s23, 32 bitop3:0xc8
	v_med3_f32 v42, v50, s19, v135
	v_med3_f32 v38, v38, s19, v135
	v_med3_f32 v26, v26, s19, v135
	v_med3_f32 v22, v22, s19, v135
	v_add_u32_e32 v2, s30, v70
	v_or_b32_e32 v6, s2, v6
	v_cvt_pk_fp8_f32 v66, v42, v38 op_sel:[0,0,1]
	v_cvt_pk_fp8_f32 v67, v26, v22 op_sel:[0,0,1]
	v_cndmask_b32_e64 v2, v6, v2, s[4:5]
	v_ashrrev_i32_e32 v6, 31, v2
	v_mul_lo_u32 v6, s6, v6
	v_mad_u64_u32 v[70:71], s[8:9], s6, v2, v[132:133]
	v_mul_lo_u32 v2, s7, v2
	v_add3_u32 v71, v2, v71, v6
	v_mul_f32_e32 v2, s31, v43
	v_mul_f32_e32 v6, s31, v47
	global_store_dwordx4 v[70:71], v[66:69], off nt
	v_med3_f32 v2, v2, s19, v135
	v_med3_f32 v6, v6, s19, v135
	v_mov_b32_e32 v66, 0
	v_cvt_pk_fp8_f32 v66, v2, v6
	v_mul_f32_e32 v10, s31, v51
	v_mul_f32_e32 v2, s31, v39
	v_med3_f32 v6, v10, s19, v135
	v_med3_f32 v2, v2, s19, v135
	v_cvt_pk_fp8_f32 v66, v6, v2 op_sel:[0,0,1]
	v_mul_f32_e32 v2, s31, v31
	v_mul_f32_e32 v6, s31, v35
	v_med3_f32 v2, v2, s19, v135
	v_med3_f32 v6, v6, s19, v135
	v_mov_b32_e32 v67, 0
	v_cvt_pk_fp8_f32 v67, v2, v6
	v_mul_f32_e32 v10, s31, v27
	v_mul_f32_e32 v2, s31, v23
	v_med3_f32 v6, v10, s19, v135
	v_med3_f32 v2, v2, s19, v135
	v_cvt_pk_fp8_f32 v67, v6, v2 op_sel:[0,0,1]
	v_mul_f32_e32 v2, s31, v11
	v_mul_f32_e32 v6, s31, v15
	v_med3_f32 v2, v2, s19, v135
	v_med3_f32 v6, v6, s19, v135
	v_mov_b32_e32 v68, 0
	v_cvt_pk_fp8_f32 v68, v2, v6
	v_mul_f32_e32 v10, s31, v19
	v_mul_f32_e32 v2, s31, v7
	v_med3_f32 v6, v10, s19, v135
	v_med3_f32 v2, v2, s19, v135
	v_cvt_pk_fp8_f32 v68, v6, v2 op_sel:[0,0,1]
	v_mul_f32_e32 v2, s31, v3
	v_mul_f32_e32 v3, s31, v55
	v_med3_f32 v2, v2, s19, v135
	v_med3_f32 v3, v3, s19, v135
	v_mov_b32_e32 v69, 0
	v_cvt_pk_fp8_f32 v69, v2, v3
	v_mul_f32_e32 v6, s31, v63
	v_mul_f32_e32 v2, s31, v59
	v_med3_f32 v3, v6, s19, v135
	v_med3_f32 v2, v2, s19, v135
	v_cvt_pk_fp8_f32 v69, v3, v2 op_sel:[0,0,1]
	v_or_b32_e32 v2, 33, v130
	v_bitop3_b32 v3, v130, s26, 33 bitop3:0xc8
	v_add_u32_e32 v2, s30, v2
	v_or_b32_e32 v3, s2, v3
	v_cndmask_b32_e64 v6, v3, v2, s[4:5]
	v_ashrrev_i32_e32 v2, 31, v6
	v_mul_lo_u32 v7, s6, v2
	v_mad_u64_u32 v[2:3], s[8:9], s6, v6, v[132:133]
	v_mul_lo_u32 v6, s7, v6
	v_add3_u32 v3, v6, v3, v7
	global_store_dwordx4 v[2:3], v[66:69], off nt
	v_mul_f32_e32 v2, s31, v44
	v_mul_f32_e32 v3, s31, v48
	v_med3_f32 v2, v2, s19, v135
	v_med3_f32 v3, v3, s19, v135
	v_mov_b32_e32 v66, 0
	v_cvt_pk_fp8_f32 v66, v2, v3
	v_mul_f32_e32 v6, s31, v52
	v_mul_f32_e32 v2, s31, v40
	v_med3_f32 v3, v6, s19, v135
	v_med3_f32 v2, v2, s19, v135
	v_cvt_pk_fp8_f32 v66, v3, v2 op_sel:[0,0,1]
	v_mul_f32_e32 v2, s31, v32
	v_mul_f32_e32 v3, s31, v36
	v_med3_f32 v2, v2, s19, v135
	v_med3_f32 v3, v3, s19, v135
	v_mov_b32_e32 v67, 0
	v_cvt_pk_fp8_f32 v67, v2, v3
	v_mul_f32_e32 v6, s31, v28
	v_mul_f32_e32 v2, s31, v24
	v_med3_f32 v3, v6, s19, v135
	v_med3_f32 v2, v2, s19, v135
	v_cvt_pk_fp8_f32 v67, v3, v2 op_sel:[0,0,1]
	v_mul_f32_e32 v2, s31, v12
	v_mul_f32_e32 v3, s31, v16
	v_med3_f32 v2, v2, s19, v135
	v_med3_f32 v3, v3, s19, v135
	v_mov_b32_e32 v68, 0
	v_cvt_pk_fp8_f32 v68, v2, v3
	v_mul_f32_e32 v6, s31, v20
	v_mul_f32_e32 v2, s31, v8
	v_med3_f32 v3, v6, s19, v135
	v_med3_f32 v2, v2, s19, v135
	v_cvt_pk_fp8_f32 v68, v3, v2 op_sel:[0,0,1]
	v_mul_f32_e32 v2, s31, v4
	v_mul_f32_e32 v3, s31, v56
	v_med3_f32 v2, v2, s19, v135
	v_med3_f32 v3, v3, s19, v135
	v_mov_b32_e32 v69, 0
	v_cvt_pk_fp8_f32 v69, v2, v3
	v_mul_f32_e32 v4, s31, v64
	v_mul_f32_e32 v2, s31, v60
	v_med3_f32 v3, v4, s19, v135
	v_med3_f32 v2, v2, s19, v135
	v_cvt_pk_fp8_f32 v69, v3, v2 op_sel:[0,0,1]
	v_or_b32_e32 v2, 34, v130
	v_bitop3_b32 v3, v130, s27, 34 bitop3:0xc8
	v_add_u32_e32 v2, s30, v2
	v_or_b32_e32 v3, s2, v3
	v_cndmask_b32_e64 v4, v3, v2, s[4:5]
	v_ashrrev_i32_e32 v2, 31, v4
	v_mul_lo_u32 v6, s6, v2
	v_mad_u64_u32 v[2:3], s[8:9], s6, v4, v[132:133]
	v_mul_lo_u32 v4, s7, v4
	v_add3_u32 v3, v4, v3, v6
	global_store_dwordx4 v[2:3], v[66:69], off nt
	v_mul_f32_e32 v2, s31, v45
	v_mul_f32_e32 v3, s31, v49
	v_med3_f32 v6, v2, s19, v135
	v_med3_f32 v3, v3, s19, v135
	v_mov_b32_e32 v2, 0
	v_cvt_pk_fp8_f32 v2, v6, v3
	v_mul_f32_e32 v4, s31, v53
	v_mul_f32_e32 v3, s31, v41
	v_med3_f32 v4, v4, s19, v135
	v_med3_f32 v3, v3, s19, v135
	v_cvt_pk_fp8_f32 v2, v4, v3 op_sel:[0,0,1]
	v_mul_f32_e32 v3, s31, v33
	v_mul_f32_e32 v4, s31, v37
	v_med3_f32 v7, v3, s19, v135
	v_med3_f32 v4, v4, s19, v135
	v_mov_b32_e32 v3, 0
	v_cvt_pk_fp8_f32 v3, v7, v4
	v_mul_f32_e32 v6, s31, v29
	v_mul_f32_e32 v4, s31, v25
	v_med3_f32 v6, v6, s19, v135
	v_med3_f32 v4, v4, s19, v135
	v_cvt_pk_fp8_f32 v3, v6, v4 op_sel:[0,0,1]
	v_mul_f32_e32 v4, s31, v13
	v_mul_f32_e32 v6, s31, v17
	v_med3_f32 v8, v4, s19, v135
	v_med3_f32 v6, v6, s19, v135
	v_mov_b32_e32 v4, 0
	v_cvt_pk_fp8_f32 v4, v8, v6
	v_mul_f32_e32 v7, s31, v21
	v_mul_f32_e32 v6, s31, v9
	v_med3_f32 v7, v7, s19, v135
	v_med3_f32 v6, v6, s19, v135
	v_cvt_pk_fp8_f32 v4, v7, v6 op_sel:[0,0,1]
	v_mul_f32_e32 v5, s31, v5
	v_mul_f32_e32 v6, s31, v57
	v_med3_f32 v8, v5, s19, v135
	v_med3_f32 v6, v6, s19, v135
	v_mov_b32_e32 v5, 0
	v_cvt_pk_fp8_f32 v5, v8, v6
	v_mul_f32_e32 v7, s31, v65
	v_mul_f32_e32 v6, s31, v61
	v_med3_f32 v7, v7, s19, v135
	v_med3_f32 v6, v6, s19, v135
	v_cvt_pk_fp8_f32 v5, v7, v6 op_sel:[0,0,1]
	v_or_b32_e32 v6, 35, v130
	v_bitop3_b32 v7, v130, s28, 35 bitop3:0xc8
	v_add_u32_e32 v6, s30, v6
	v_or_b32_e32 v7, s2, v7
	v_cndmask_b32_e64 v8, v7, v6, s[4:5]
	v_ashrrev_i32_e32 v6, 31, v8
	v_mul_lo_u32 v9, s6, v6
	v_mad_u64_u32 v[6:7], s[4:5], s6, v8, v[132:133]
	v_mul_lo_u32 v8, s7, v8
	v_add3_u32 v7, v8, v7, v9
	global_store_dwordx4 v[6:7], v[2:5], off nt
	s_cbranch_scc0 .LBB0_246

; __device__ __forceinline__ void moe_convert(Frame& F, int lo, int hi, int rank, int nrank) {
;     ...
;     for (int it = lo + rank; it < hi; it += nrank) {
;         int r = it; const float* W; unsigned char* WT; int N, ldt, kind, off; float f8s;
;         if (r < 14336) { const int e = r / 1792; r -= e * 1792; W = F.in[IN_WMG] + (size_t)e * 2048 * DFFE; N = DFFE; WT = F.ws + WS_WGU1 + (size_t)e * 14336 * 2048; ldt = 2048; kind = 1; off = 0; f8s = 32.f; }
;         else if ((r -= 14336) < 14336) { const int e = r / 1792; r -= e * 1792; W = F.in[IN_WMU] + (size_t)e * 2048 * DFFE; N = DFFE; WT = F.ws + WS_WGU1 + (size_t)e * 14336 * 2048; ldt = 2048; kind = 1; off = 128; f8s = 256.f; }
;         else { r -= 14336; const int e = r / 1792; r -= e * 1792; W = F.in[IN_WMD] + (size_t)e * DFFE * 2048; N = 2048; WT = F.ws + WS_WDN1 + (size_t)e * 2048 * DFFE; ldt = DFFE; kind = 0; off = 0; f8s = 64.f; }
;         transpose_item_f8(W, N, WT, ldt, kind, off, r, F.lane, f8s);
.Lsf0_notw0:
	s_cmp_gt_u32 s4, 4
	s_cbranch_scc1 .Lsf0_skip
	v_mov_b32_e32 v8, 0x20020
	ds_read_b32 v9, v8 offset:4
	v_mbcnt_lo_u32_b32 v2, -1, 0
	v_mbcnt_hi_u32_b32 v2, -1, v2
	s_waitcnt lgkmcnt(0)
	v_readfirstlane_b32 s5, v9
	s_cmp_ge_u32 s5, 64
	s_cbranch_scc1 .Lsf0_skip
	s_add_i32 s5, s4, -1
	s_lshl_b32 s5, s5, 14
	v_lshl_add_u32 v7, v2, 4, s5
	ds_write_b128 v7, v[160:163] offset:0
	ds_write_b128 v7, v[164:167] offset:1024
	ds_write_b128 v7, v[168:171] offset:2048
	ds_write_b128 v7, v[172:175] offset:3072
	ds_write_b128 v7, v[176:179] offset:4096
	ds_write_b128 v7, v[180:183] offset:5120
	ds_write_b128 v7, v[184:187] offset:6144
	ds_write_b128 v7, v[188:191] offset:7168
	ds_write_b128 v7, v[192:195] offset:8192
	ds_write_b128 v7, v[196:199] offset:9216
	ds_write_b128 v7, v[200:203] offset:10240
	ds_write_b128 v7, v[204:207] offset:11264
	ds_write_b128 v7, v[208:211] offset:12288
	ds_write_b128 v7, v[212:215] offset:13312
	ds_write_b128 v7, v[216:219] offset:14336
	ds_write_b128 v7, v[220:223] offset:15360
	v_readlane_b32 s6, v247, 0
	v_readlane_b32 s7, v247, 1
	s_load_dwordx2 s[10:11], s[6:7], 0xc0
	s_load_dwordx2 s[12:13], s[6:7], 0xc8
	v_readlane_b32 s33, v247, 6
	v_mov_b32_e32 v3, 0x43e00000
	v_cmp_eq_u32_e32 vcc, 0, v2
	s_mul_i32 s33, s33, 64
	s_nop 1
	v_cndmask_b32_e64 v18, 0, 1, vcc
	s_waitcnt lgkmcnt(0)
	s_mov_b32 s34, 1
.Lsf0_loop:
	ds_read_b32 v9, v8
	s_waitcnt lgkmcnt(0)
	v_readfirstlane_b32 s5, v9
	s_cmp_eq_u32 s5, 1
	s_cbranch_scc1 .Lsf0_done
	ds_add_rtn_u32 v9, v8, v18 offset:4
	s_waitcnt lgkmcnt(0)
	v_readfirstlane_b32 s18, v9
	s_cmp_ge_u32 s18, 64
	s_cbranch_scc1 .Lsf0_done
	s_add_i32 s18, s18, s33
	s_and_b32 s27, s18, 1
	s_lshr_b32 s19, s18, 1
	s_add_i32 s19, s19, 0x6800
	s_cmp_lt_u32 s19, 0x7000
	s_cbranch_scc0 .Lsf0_down
	s_add_i32 s20, s19, 0xffffc800
	s_lshr_b32 s21, s20, 8
	s_mul_i32 s21, s21, 37
	s_lshr_b32 s21, s21, 8
	s_mul_i32 s28, s21, 0x700
	s_sub_i32 s20, s20, s28
	s_mul_i32 s28, s21, 0x3800000
	s_add_u32 s14, s10, s28
	s_addc_u32 s15, s11, 0
	s_mul_i32 s28, s21, 0x1c00000
	s_add_u32 s28, s28, 0x7800000
	s_add_u32 s16, s86, s28
	s_addc_u32 s17, s87, 0
	s_movk_i32 s24, 0x7000
	s_movk_i32 s25, 0x800
	s_mov_b32 s26, 0x43800000
	s_lshr_b32 s22, s20, 4
	s_mul_i32 s22, s22, 0x2493
	s_lshr_b32 s22, s22, 16
	s_mul_i32 s28, s22, 0x70
	s_sub_i32 s23, s20, s28
	s_mov_b32 s29, 1
	s_branch .Lsf0_dec

; __device__ __forceinline__ void transpose_item_f8(const float* W, int N, unsigned char* WT, int ldt, int kind, int off, int item, int lane, float scale) {
;     const int nblk = N >> 6, kb = item / nblk, nb = item - kb * nblk, k0 = 128 * kb + 16 * (lane & 7), n = 64 * nb + 4 * (lane >> 3);
;     const f32x4* src = (const f32x4*)(W + (size_t)k0 * N + n);
;     f32x4 v[2][16];
; #pragma unroll
;     for (int hh = 0; hh < 2; ++hh)
; #pragma unroll
;         for (int j = 0; j < 16; ++j) v[hh][j] = __builtin_nontemporal_load(src + (size_t)j * (N >> 2) + 8 * hh);
.Lsf0_k0:
	s_mul_i32 s30, s30, s25
	s_lshl_b32 s31, s22, 7
	s_add_i32 s30, s30, s31
	s_add_u32 s16, s16, s30
	s_addc_u32 s17, s17, 0
	v_lshrrev_b32_e32 v6, 3, v2
	v_lshlrev_b32_e32 v6, 2, v6
	v_mul_lo_u32 v6, s25, v6
	v_lshl_add_u32 v6, v4, 4, v6
	global_load_dwordx4 v[160:163], v5, s[14:15] nt
	s_add_u32 s14, s14, s24
	s_addc_u32 s15, s15, 0
	global_load_dwordx4 v[164:167], v5, s[14:15] nt
	s_add_u32 s14, s14, s24
	s_addc_u32 s15, s15, 0
	global_load_dwordx4 v[168:171], v5, s[14:15] nt
	s_add_u32 s14, s14, s24
	s_addc_u32 s15, s15, 0
	global_load_dwordx4 v[172:175], v5, s[14:15] nt
	s_add_u32 s14, s14, s24
	s_addc_u32 s15, s15, 0
	global_load_dwordx4 v[176:179], v5, s[14:15] nt
	s_add_u32 s14, s14, s24
	s_addc_u32 s15, s15, 0
	global_load_dwordx4 v[180:183], v5, s[14:15] nt
	s_add_u32 s14, s14, s24
	s_addc_u32 s15, s15, 0
	global_load_dwordx4 v[184:187], v5, s[14:15] nt
	s_add_u32 s14, s14, s24
	s_addc_u32 s15, s15, 0
	global_load_dwordx4 v[188:191], v5, s[14:15] nt
	s_add_u32 s14, s14, s24
	s_addc_u32 s15, s15, 0
	global_load_dwordx4 v[192:195], v5, s[14:15] nt
	s_add_u32 s14, s14, s24
	s_addc_u32 s15, s15, 0
	global_load_dwordx4 v[196:199], v5, s[14:15] nt
	s_add_u32 s14, s14, s24
	s_addc_u32 s15, s15, 0
	global_load_dwordx4 v[200:203], v5, s[14:15] nt
	s_add_u32 s14, s14, s24
	s_addc_u32 s15, s15, 0
	global_load_dwordx4 v[204:207], v5, s[14:15] nt
	s_add_u32 s14, s14, s24
	s_addc_u32 s15, s15, 0
	global_load_dwordx4 v[208:211], v5, s[14:15] nt
	s_add_u32 s14, s14, s24
	s_addc_u32 s15, s15, 0
	global_load_dwordx4 v[212:215], v5, s[14:15] nt
	s_add_u32 s14, s14, s24
	s_addc_u32 s15, s15, 0
	global_load_dwordx4 v[216:219], v5, s[14:15] nt
	s_add_u32 s14, s14, s24
	s_addc_u32 s15, s15, 0
	global_load_dwordx4 v[220:223], v5, s[14:15] nt
	s_mov_b32 s28, 0xc3e00000
	s_waitcnt vmcnt(0)
; __device__ __forceinline__ unsigned pk4_fp8(float a, float b, float c, float d) { int w = 0; w = __builtin_amdgcn_cvt_pk_fp8_f32(clamp448(a), clamp448(b), w, false); w = __builtin_amdgcn_cvt_pk_fp8_f32(clamp448(c), clamp448(d), w, true); return (unsigned)w; }
; __device__ __forceinline__ void transpose_item_f8(const float* W, int N, unsigned char* WT, int ldt, int kind, int off, int item, int lane, float scale) {
;     ...
; #pragma unroll
;     for (int hh = 0; hh < 2; ++hh)
; #pragma unroll
;         for (int i = 0; i < 4; ++i) { v4u o; o.x = pg8::pk4_fp8(v[hh][0][i] * scale, v[hh][1][i] * scale, v[hh][2][i] * scale, v[hh][3][i] * scale); o.y = pg8::pk4_fp8(v[hh][4][i] * scale, v[hh][5][i] * scale, v[hh][6][i] * scale, v[hh][7][i] * scale);
;             o.z = pg8::pk4_fp8(v[hh][8][i] * scale, v[hh][9][i] * scale, v[hh][10][i] * scale, v[hh][11][i] * scale); o.w = pg8::pk4_fp8(v[hh][12][i] * scale, v[hh][13][i] * scale, v[hh][14][i] * scale, v[hh][15][i] * scale);
;             __builtin_nontemporal_store(o, (v4u*)(WT + (size_t)rowmap(kind, off, n + 32 * hh + i) * ldt + k0)); }
	v_mul_f32_e32 v160, s26, v160
	v_mul_f32_e32 v161, s26, v161
	v_mul_f32_e32 v162, s26, v162
	v_mul_f32_e32 v163, s26, v163
	v_mul_f32_e32 v164, s26, v164
	v_mul_f32_e32 v165, s26, v165
	v_mul_f32_e32 v166, s26, v166
	v_mul_f32_e32 v167, s26, v167
	v_mul_f32_e32 v168, s26, v168
	v_mul_f32_e32 v169, s26, v169
	v_mul_f32_e32 v170, s26, v170
	v_mul_f32_e32 v171, s26, v171
	v_mul_f32_e32 v172, s26, v172
	v_mul_f32_e32 v173, s26, v173
	v_mul_f32_e32 v174, s26, v174
	v_mul_f32_e32 v175, s26, v175
	v_mul_f32_e32 v176, s26, v176
	v_mul_f32_e32 v177, s26, v177
	v_mul_f32_e32 v178, s26, v178
	v_mul_f32_e32 v179, s26, v179
	v_mul_f32_e32 v180, s26, v180
	v_mul_f32_e32 v181, s26, v181
	v_mul_f32_e32 v182, s26, v182
	v_mul_f32_e32 v183, s26, v183
	v_mul_f32_e32 v184, s26, v184
	v_mul_f32_e32 v185, s26, v185
	v_mul_f32_e32 v186, s26, v186
	v_mul_f32_e32 v187, s26, v187
	v_mul_f32_e32 v188, s26, v188
	v_mul_f32_e32 v189, s26, v189
	v_mul_f32_e32 v190, s26, v190
	v_mul_f32_e32 v191, s26, v191
	v_mul_f32_e32 v192, s26, v192
	v_mul_f32_e32 v193, s26, v193
	v_mul_f32_e32 v194, s26, v194
	v_mul_f32_e32 v195, s26, v195
	v_mul_f32_e32 v196, s26, v196
	v_mul_f32_e32 v197, s26, v197
	v_mul_f32_e32 v198, s26, v198
	v_mul_f32_e32 v199, s26, v199
	v_mul_f32_e32 v200, s26, v200
	v_mul_f32_e32 v201, s26, v201
	v_mul_f32_e32 v202, s26, v202
	v_mul_f32_e32 v203, s26, v203
	v_mul_f32_e32 v204, s26, v204
	v_mul_f32_e32 v205, s26, v205
	v_mul_f32_e32 v206, s26, v206
	v_mul_f32_e32 v207, s26, v207
	v_mul_f32_e32 v208, s26, v208
	v_mul_f32_e32 v209, s26, v209
	v_mul_f32_e32 v210, s26, v210
	v_mul_f32_e32 v211, s26, v211
	v_mul_f32_e32 v212, s26, v212
	v_mul_f32_e32 v213, s26, v213
	v_mul_f32_e32 v214, s26, v214
	v_mul_f32_e32 v215, s26, v215
	v_mul_f32_e32 v216, s26, v216
	v_mul_f32_e32 v217, s26, v217
	v_mul_f32_e32 v218, s26, v218
	v_mul_f32_e32 v219, s26, v219
	v_mul_f32_e32 v220, s26, v220
	v_mul_f32_e32 v221, s26, v221
	v_mul_f32_e32 v222, s26, v222
	v_mul_f32_e32 v223, s26, v223
	v_med3_f32 v160, v160, s28, v3
	v_med3_f32 v161, v161, s28, v3
	v_med3_f32 v162, v162, s28, v3
	v_med3_f32 v163, v163, s28, v3
	v_med3_f32 v164, v164, s28, v3
	v_med3_f32 v165, v165, s28, v3
	v_med3_f32 v166, v166, s28, v3
	v_med3_f32 v167, v167, s28, v3
	v_med3_f32 v168, v168, s28, v3
	v_med3_f32 v169, v169, s28, v3
	v_med3_f32 v170, v170, s28, v3
	v_med3_f32 v171, v171, s28, v3
	v_med3_f32 v172, v172, s28, v3
	v_med3_f32 v173, v173, s28, v3
	v_med3_f32 v174, v174, s28, v3
	v_med3_f32 v175, v175, s28, v3
	v_med3_f32 v176, v176, s28, v3
	v_med3_f32 v177, v177, s28, v3
	v_med3_f32 v178, v178, s28, v3
	v_med3_f32 v179, v179, s28, v3
	v_med3_f32 v180, v180, s28, v3
	v_med3_f32 v181, v181, s28, v3
	v_med3_f32 v182, v182, s28, v3
	v_med3_f32 v183, v183, s28, v3
	v_med3_f32 v184, v184, s28, v3
	v_med3_f32 v185, v185, s28, v3
	v_med3_f32 v186, v186, s28, v3
	v_med3_f32 v187, v187, s28, v3
	v_med3_f32 v188, v188, s28, v3
	v_med3_f32 v189, v189, s28, v3
	v_med3_f32 v190, v190, s28, v3
	v_med3_f32 v191, v191, s28, v3
	v_med3_f32 v192, v192, s28, v3
	v_med3_f32 v193, v193, s28, v3
	v_med3_f32 v194, v194, s28, v3
	v_med3_f32 v195, v195, s28, v3
	v_med3_f32 v196, v196, s28, v3
	v_med3_f32 v197, v197, s28, v3
	v_med3_f32 v198, v198, s28, v3
	v_med3_f32 v199, v199, s28, v3
	v_med3_f32 v200, v200, s28, v3
	v_med3_f32 v201, v201, s28, v3
	v_med3_f32 v202, v202, s28, v3
	v_med3_f32 v203, v203, s28, v3
	v_med3_f32 v204, v204, s28, v3
	v_med3_f32 v205, v205, s28, v3
	v_med3_f32 v206, v206, s28, v3
	v_med3_f32 v207, v207, s28, v3
	v_med3_f32 v208, v208, s28, v3
	v_med3_f32 v209, v209, s28, v3
	v_med3_f32 v210, v210, s28, v3
	v_med3_f32 v211, v211, s28, v3
	v_med3_f32 v212, v212, s28, v3
	v_med3_f32 v213, v213, s28, v3
	v_med3_f32 v214, v214, s28, v3
	v_med3_f32 v215, v215, s28, v3
	v_med3_f32 v216, v216, s28, v3
	v_med3_f32 v217, v217, s28, v3
	v_med3_f32 v218, v218, s28, v3
	v_med3_f32 v219, v219, s28, v3
	v_med3_f32 v220, v220, s28, v3
	v_med3_f32 v221, v221, s28, v3
	v_med3_f32 v222, v222, s28, v3
	v_med3_f32 v223, v223, s28, v3
	v_mov_b32_e32 v10, 0
	v_mov_b32_e32 v11, 0
	v_mov_b32_e32 v12, 0
	v_mov_b32_e32 v13, 0
	v_cvt_pk_fp8_f32 v10, v160, v164
	v_cvt_pk_fp8_f32 v11, v176, v180
	v_cvt_pk_fp8_f32 v12, v192, v196
	v_cvt_pk_fp8_f32 v13, v208, v212
	v_cvt_pk_fp8_f32 v10, v168, v172 op_sel:[0,0,1]
	v_cvt_pk_fp8_f32 v11, v184, v188 op_sel:[0,0,1]
	v_cvt_pk_fp8_f32 v12, v200, v204 op_sel:[0,0,1]
	v_cvt_pk_fp8_f32 v13, v216, v220 op_sel:[0,0,1]
	s_nop 1
	global_store_dwordx4 v6, v[10:13], s[16:17] nt
	s_add_u32 s16, s16, s25
	s_addc_u32 s17, s17, 0
	v_mov_b32_e32 v14, 0
	v_mov_b32_e32 v15, 0
	v_mov_b32_e32 v16, 0
	v_mov_b32_e32 v17, 0
	v_cvt_pk_fp8_f32 v14, v161, v165
	v_cvt_pk_fp8_f32 v15, v177, v181
	v_cvt_pk_fp8_f32 v16, v193, v197
	v_cvt_pk_fp8_f32 v17, v209, v213
	v_cvt_pk_fp8_f32 v14, v169, v173 op_sel:[0,0,1]
	v_cvt_pk_fp8_f32 v15, v185, v189 op_sel:[0,0,1]
	v_cvt_pk_fp8_f32 v16, v201, v205 op_sel:[0,0,1]
	v_cvt_pk_fp8_f32 v17, v217, v221 op_sel:[0,0,1]
	s_nop 1
	global_store_dwordx4 v6, v[14:17], s[16:17] nt
	s_add_u32 s16, s16, s25
	s_addc_u32 s17, s17, 0
	v_mov_b32_e32 v248, 0
	v_mov_b32_e32 v249, 0
	v_mov_b32_e32 v250, 0
	v_mov_b32_e32 v251, 0
	v_cvt_pk_fp8_f32 v248, v162, v166
	v_cvt_pk_fp8_f32 v249, v178, v182
	v_cvt_pk_fp8_f32 v250, v194, v198
	v_cvt_pk_fp8_f32 v251, v210, v214
	v_cvt_pk_fp8_f32 v248, v170, v174 op_sel:[0,0,1]
	v_cvt_pk_fp8_f32 v249, v186, v190 op_sel:[0,0,1]
	v_cvt_pk_fp8_f32 v250, v202, v206 op_sel:[0,0,1]
	v_cvt_pk_fp8_f32 v251, v218, v222 op_sel:[0,0,1]
	s_nop 1
	global_store_dwordx4 v6, v[248:251], s[16:17] nt
	s_add_u32 s16, s16, s25
	s_addc_u32 s17, s17, 0
	v_mov_b32_e32 v252, 0
	v_mov_b32_e32 v253, 0
	v_mov_b32_e32 v254, 0
	v_mov_b32_e32 v255, 0
	v_cvt_pk_fp8_f32 v252, v163, v167
	v_cvt_pk_fp8_f32 v253, v179, v183
	v_cvt_pk_fp8_f32 v254, v195, v199
	v_cvt_pk_fp8_f32 v255, v211, v215
	v_cvt_pk_fp8_f32 v252, v171, v175 op_sel:[0,0,1]
	v_cvt_pk_fp8_f32 v253, v187, v191 op_sel:[0,0,1]
	v_cvt_pk_fp8_f32 v254, v203, v207 op_sel:[0,0,1]
	v_cvt_pk_fp8_f32 v255, v219, v223 op_sel:[0,0,1]
	s_nop 1
	global_store_dwordx4 v6, v[252:255], s[16:17] nt
	s_sub_u32 s34, s34, 1
	s_cmp_eq_u32 s34, 0
	s_cbranch_scc1 .Lsf0_done
	s_branch .Lsf0_loop
.Lsf0_done:
	ds_read_b128 v[160:163], v7 offset:0
	ds_read_b128 v[164:167], v7 offset:1024
	ds_read_b128 v[168:171], v7 offset:2048
	ds_read_b128 v[172:175], v7 offset:3072
	ds_read_b128 v[176:179], v7 offset:4096
	ds_read_b128 v[180:183], v7 offset:5120
	ds_read_b128 v[184:187], v7 offset:6144
	ds_read_b128 v[188:191], v7 offset:7168
	ds_read_b128 v[192:195], v7 offset:8192
	ds_read_b128 v[196:199], v7 offset:9216
	ds_read_b128 v[200:203], v7 offset:10240
	ds_read_b128 v[204:207], v7 offset:11264
	ds_read_b128 v[208:211], v7 offset:12288
	ds_read_b128 v[212:215], v7 offset:13312
	ds_read_b128 v[216:219], v7 offset:14336
	ds_read_b128 v[220:223], v7 offset:15360

; __device__ __forceinline__ void transpose_item_f8(const float* W, int N, unsigned char* WT, int ldt, int kind, int off, int item, int lane, float scale) {
;     const int nblk = N >> 6, kb = item / nblk, nb = item - kb * nblk, k0 = 128 * kb + 16 * (lane & 7), n = 64 * nb + 4 * (lane >> 3);
; __device__ __forceinline__ void moe_convert(Frame& F, int lo, int hi, int rank, int nrank) {
;     ...
;     for (int it = lo + rank; it < hi; it += nrank) {
;         int r = it; const float* W; unsigned char* WT; int N, ldt, kind, off; float f8s;
;         if (r < 14336) { const int e = r / 1792; r -= e * 1792; W = F.in[IN_WMG] + (size_t)e * 2048 * DFFE; N = DFFE; WT = F.ws + WS_WGU1 + (size_t)e * 14336 * 2048; ldt = 2048; kind = 1; off = 0; f8s = 32.f; }
;         else if ((r -= 14336) < 14336) { const int e = r / 1792; r -= e * 1792; W = F.in[IN_WMU] + (size_t)e * 2048 * DFFE; N = DFFE; WT = F.ws + WS_WGU1 + (size_t)e * 14336 * 2048; ldt = 2048; kind = 1; off = 128; f8s = 256.f; }
;         else { r -= 14336; const int e = r / 1792; r -= e * 1792; W = F.in[IN_WMD] + (size_t)e * DFFE * 2048; N = 2048; WT = F.ws + WS_WDN1 + (size_t)e * 2048 * DFFE; ldt = DFFE; kind = 0; off = 0; f8s = 64.f; }
;         transpose_item_f8(W, N, WT, ldt, kind, off, r, F.lane, f8s);
.Lsf1_loop:
	ds_read_b32 v9, v8
	s_waitcnt lgkmcnt(0)
	v_readfirstlane_b32 s5, v9
	s_cmp_eq_u32 s5, 2
	s_cbranch_scc1 .Lsf1_done
	ds_add_rtn_u32 v9, v8, v18 offset:4
	s_waitcnt lgkmcnt(0)
	v_readfirstlane_b32 s18, v9
	s_cmp_ge_u32 s18, 64
	s_cbranch_scc1 .Lsf1_done
	s_add_i32 s18, s18, s33
	s_and_b32 s27, s18, 1
	s_lshr_b32 s19, s18, 1
	s_add_i32 s19, s19, 0x6800
	s_cmp_lt_u32 s19, 0x7000
	s_cbranch_scc0 .Lsf1_down
	s_add_i32 s20, s19, 0xffffc800
	s_lshr_b32 s21, s20, 8
	s_mul_i32 s21, s21, 37
	s_lshr_b32 s21, s21, 8
	s_mul_i32 s28, s21, 0x700
	s_sub_i32 s20, s20, s28
	s_mul_i32 s28, s21, 0x3800000
	s_add_u32 s14, s10, s28
	s_addc_u32 s15, s11, 0
	s_mul_i32 s28, s21, 0x1c00000
	s_add_u32 s28, s28, 0x7800000
	s_add_u32 s16, s86, s28
	s_addc_u32 s17, s87, 0
	s_movk_i32 s24, 0x7000
	s_movk_i32 s25, 0x800
	s_mov_b32 s26, 0x43800000
	s_lshr_b32 s22, s20, 4
	s_mul_i32 s22, s22, 0x2493
	s_lshr_b32 s22, s22, 16
	s_mul_i32 s28, s22, 0x70
	s_sub_i32 s23, s20, s28
	s_mov_b32 s29, 1
	s_branch .Lsf1_dec

; __device__ __forceinline__ void transpose_item_f8(const float* W, int N, unsigned char* WT, int ldt, int kind, int off, int item, int lane, float scale) {
;     const int nblk = N >> 6, kb = item / nblk, nb = item - kb * nblk, k0 = 128 * kb + 16 * (lane & 7), n = 64 * nb + 4 * (lane >> 3);
; __device__ __forceinline__ void moe_convert(Frame& F, int lo, int hi, int rank, int nrank) {
;     ...
;     for (int it = lo + rank; it < hi; it += nrank) {
;         int r = it; const float* W; unsigned char* WT; int N, ldt, kind, off; float f8s;
;         if (r < 14336) { const int e = r / 1792; r -= e * 1792; W = F.in[IN_WMG] + (size_t)e * 2048 * DFFE; N = DFFE; WT = F.ws + WS_WGU1 + (size_t)e * 14336 * 2048; ldt = 2048; kind = 1; off = 0; f8s = 32.f; }
;         else if ((r -= 14336) < 14336) { const int e = r / 1792; r -= e * 1792; W = F.in[IN_WMU] + (size_t)e * 2048 * DFFE; N = DFFE; WT = F.ws + WS_WGU1 + (size_t)e * 14336 * 2048; ldt = 2048; kind = 1; off = 128; f8s = 256.f; }
;         else { r -= 14336; const int e = r / 1792; r -= e * 1792; W = F.in[IN_WMD] + (size_t)e * DFFE * 2048; N = 2048; WT = F.ws + WS_WDN1 + (size_t)e * 2048 * DFFE; ldt = DFFE; kind = 0; off = 0; f8s = 64.f; }
;         transpose_item_f8(W, N, WT, ldt, kind, off, r, F.lane, f8s);
.Lsf2_loop:
	ds_read_b32 v9, v8
	s_waitcnt lgkmcnt(0)
	v_readfirstlane_b32 s5, v9
	s_cmp_eq_u32 s5, 3
	s_cbranch_scc1 .Lsf2_done
	ds_add_rtn_u32 v9, v8, v18 offset:4
	s_waitcnt lgkmcnt(0)
	v_readfirstlane_b32 s18, v9
	s_cmp_ge_u32 s18, 64
	s_cbranch_scc1 .Lsf2_done
	s_add_i32 s18, s18, s33
	s_and_b32 s27, s18, 1
	s_lshr_b32 s19, s18, 1
	s_add_i32 s19, s19, 0x6800
	s_cmp_lt_u32 s19, 0x7000
	s_cbranch_scc0 .Lsf2_down
	s_add_i32 s20, s19, 0xffffc800
	s_lshr_b32 s21, s20, 8
	s_mul_i32 s21, s21, 37
	s_lshr_b32 s21, s21, 8
	s_mul_i32 s28, s21, 0x700
	s_sub_i32 s20, s20, s28
	s_mul_i32 s28, s21, 0x3800000
	s_add_u32 s14, s10, s28
	s_addc_u32 s15, s11, 0
	s_mul_i32 s28, s21, 0x1c00000
	s_add_u32 s28, s28, 0x7800000
	s_add_u32 s16, s86, s28
	s_addc_u32 s17, s87, 0
	s_movk_i32 s24, 0x7000
	s_movk_i32 s25, 0x800
	s_mov_b32 s26, 0x43800000
	s_lshr_b32 s22, s20, 4
	s_mul_i32 s22, s22, 0x2493
	s_lshr_b32 s22, s22, 16
	s_mul_i32 s28, s22, 0x70
	s_sub_i32 s23, s20, s28
	s_mov_b32 s29, 1
	s_branch .Lsf2_dec

; __device__ __forceinline__ void transpose_item_f8(const float* W, int N, unsigned char* WT, int ldt, int kind, int off, int item, int lane, float scale) {
;     const int nblk = N >> 6, kb = item / nblk, nb = item - kb * nblk, k0 = 128 * kb + 16 * (lane & 7), n = 64 * nb + 4 * (lane >> 3);
; __device__ __forceinline__ void moe_convert(Frame& F, int lo, int hi, int rank, int nrank) {
;     ...
;     for (int it = lo + rank; it < hi; it += nrank) {
;         int r = it; const float* W; unsigned char* WT; int N, ldt, kind, off; float f8s;
;         if (r < 14336) { const int e = r / 1792; r -= e * 1792; W = F.in[IN_WMG] + (size_t)e * 2048 * DFFE; N = DFFE; WT = F.ws + WS_WGU1 + (size_t)e * 14336 * 2048; ldt = 2048; kind = 1; off = 0; f8s = 32.f; }
;         else if ((r -= 14336) < 14336) { const int e = r / 1792; r -= e * 1792; W = F.in[IN_WMU] + (size_t)e * 2048 * DFFE; N = DFFE; WT = F.ws + WS_WGU1 + (size_t)e * 14336 * 2048; ldt = 2048; kind = 1; off = 128; f8s = 256.f; }
;         else { r -= 14336; const int e = r / 1792; r -= e * 1792; W = F.in[IN_WMD] + (size_t)e * DFFE * 2048; N = 2048; WT = F.ws + WS_WDN1 + (size_t)e * 2048 * DFFE; ldt = DFFE; kind = 0; off = 0; f8s = 64.f; }
;         transpose_item_f8(W, N, WT, ldt, kind, off, r, F.lane, f8s);
.Lsf3_loop:
	ds_read_b32 v9, v8
	s_waitcnt lgkmcnt(0)
	v_readfirstlane_b32 s5, v9
	s_cmp_eq_u32 s5, 4
	s_cbranch_scc1 .Lsf3_done
	ds_add_rtn_u32 v9, v8, v18 offset:4
	s_waitcnt lgkmcnt(0)
	v_readfirstlane_b32 s18, v9
	s_cmp_ge_u32 s18, 64
	s_cbranch_scc1 .Lsf3_done
	s_add_i32 s18, s18, s33
	s_and_b32 s27, s18, 1
	s_lshr_b32 s19, s18, 1
	s_add_i32 s19, s19, 0x6800
	s_cmp_lt_u32 s19, 0x7000
	s_cbranch_scc0 .Lsf3_down
	s_add_i32 s20, s19, 0xffffc800
	s_lshr_b32 s21, s20, 8
	s_mul_i32 s21, s21, 37
	s_lshr_b32 s21, s21, 8
	s_mul_i32 s28, s21, 0x700
	s_sub_i32 s20, s20, s28
	s_mul_i32 s28, s21, 0x3800000
	s_add_u32 s14, s10, s28
	s_addc_u32 s15, s11, 0
	s_mul_i32 s28, s21, 0x1c00000
	s_add_u32 s28, s28, 0x7800000
	s_add_u32 s16, s86, s28
	s_addc_u32 s17, s87, 0
	s_movk_i32 s24, 0x7000
	s_movk_i32 s25, 0x800
	s_mov_b32 s26, 0x43800000
	s_lshr_b32 s22, s20, 4
	s_mul_i32 s22, s22, 0x2493
	s_lshr_b32 s22, s22, 16
	s_mul_i32 s28, s22, 0x70
	s_sub_i32 s23, s20, s28
	s_mov_b32 s29, 1
	s_branch .Lsf3_dec

; __device__ __forceinline__ void transpose_item_f8(const float* W, int N, unsigned char* WT, int ldt, int kind, int off, int item, int lane, float scale) {
;     const int nblk = N >> 6, kb = item / nblk, nb = item - kb * nblk, k0 = 128 * kb + 16 * (lane & 7), n = 64 * nb + 4 * (lane >> 3);
; __device__ __forceinline__ void moe_convert(Frame& F, int lo, int hi, int rank, int nrank) {
;     ...
;     for (int it = lo + rank; it < hi; it += nrank) {
;         int r = it; const float* W; unsigned char* WT; int N, ldt, kind, off; float f8s;
;         if (r < 14336) { const int e = r / 1792; r -= e * 1792; W = F.in[IN_WMG] + (size_t)e * 2048 * DFFE; N = DFFE; WT = F.ws + WS_WGU1 + (size_t)e * 14336 * 2048; ldt = 2048; kind = 1; off = 0; f8s = 32.f; }
;         else if ((r -= 14336) < 14336) { const int e = r / 1792; r -= e * 1792; W = F.in[IN_WMU] + (size_t)e * 2048 * DFFE; N = DFFE; WT = F.ws + WS_WGU1 + (size_t)e * 14336 * 2048; ldt = 2048; kind = 1; off = 128; f8s = 256.f; }
;         else { r -= 14336; const int e = r / 1792; r -= e * 1792; W = F.in[IN_WMD] + (size_t)e * DFFE * 2048; N = 2048; WT = F.ws + WS_WDN1 + (size_t)e * 2048 * DFFE; ldt = DFFE; kind = 0; off = 0; f8s = 64.f; }
;         transpose_item_f8(W, N, WT, ldt, kind, off, r, F.lane, f8s);
.Lsf4_loop:
	ds_read_b32 v9, v8
	s_waitcnt lgkmcnt(0)
	v_readfirstlane_b32 s5, v9
	s_cmp_eq_u32 s5, 5
	s_cbranch_scc1 .Lsf4_done
	ds_add_rtn_u32 v9, v8, v18 offset:4
	s_waitcnt lgkmcnt(0)
	v_readfirstlane_b32 s18, v9
	s_cmp_ge_u32 s18, 64
	s_cbranch_scc1 .Lsf4_done
	s_add_i32 s18, s18, s33
	s_and_b32 s27, s18, 1
	s_lshr_b32 s19, s18, 1
	s_add_i32 s19, s19, 0x6800
	s_cmp_lt_u32 s19, 0x7000
	s_cbranch_scc0 .Lsf4_down
	s_add_i32 s20, s19, 0xffffc800
	s_lshr_b32 s21, s20, 8
	s_mul_i32 s21, s21, 37
	s_lshr_b32 s21, s21, 8
	s_mul_i32 s28, s21, 0x700
	s_sub_i32 s20, s20, s28
	s_mul_i32 s28, s21, 0x3800000
	s_add_u32 s14, s10, s28
	s_addc_u32 s15, s11, 0
	s_mul_i32 s28, s21, 0x1c00000
	s_add_u32 s28, s28, 0x7800000
	s_add_u32 s16, s86, s28
	s_addc_u32 s17, s87, 0
	s_movk_i32 s24, 0x7000
	s_movk_i32 s25, 0x800
	s_mov_b32 s26, 0x43800000
	s_lshr_b32 s22, s20, 4
	s_mul_i32 s22, s22, 0x2493
	s_lshr_b32 s22, s22, 16
	s_mul_i32 s28, s22, 0x70
	s_sub_i32 s23, s20, s28
	s_mov_b32 s29, 1
	s_branch .Lsf4_dec

; __device__ __forceinline__ void transpose_item_f8(const float* W, int N, unsigned char* WT, int ldt, int kind, int off, int item, int lane, float scale) {
;     const int nblk = N >> 6, kb = item / nblk, nb = item - kb * nblk, k0 = 128 * kb + 16 * (lane & 7), n = 64 * nb + 4 * (lane >> 3);
; __device__ __forceinline__ void moe_convert(Frame& F, int lo, int hi, int rank, int nrank) {
;     ...
;     for (int it = lo + rank; it < hi; it += nrank) {
;         int r = it; const float* W; unsigned char* WT; int N, ldt, kind, off; float f8s;
;         if (r < 14336) { const int e = r / 1792; r -= e * 1792; W = F.in[IN_WMG] + (size_t)e * 2048 * DFFE; N = DFFE; WT = F.ws + WS_WGU1 + (size_t)e * 14336 * 2048; ldt = 2048; kind = 1; off = 0; f8s = 32.f; }
;         else if ((r -= 14336) < 14336) { const int e = r / 1792; r -= e * 1792; W = F.in[IN_WMU] + (size_t)e * 2048 * DFFE; N = DFFE; WT = F.ws + WS_WGU1 + (size_t)e * 14336 * 2048; ldt = 2048; kind = 1; off = 128; f8s = 256.f; }
;         else { r -= 14336; const int e = r / 1792; r -= e * 1792; W = F.in[IN_WMD] + (size_t)e * DFFE * 2048; N = 2048; WT = F.ws + WS_WDN1 + (size_t)e * 2048 * DFFE; ldt = DFFE; kind = 0; off = 0; f8s = 64.f; }
;         transpose_item_f8(W, N, WT, ldt, kind, off, r, F.lane, f8s);
.Lsf5_loop:
	ds_read_b32 v9, v8
	s_waitcnt lgkmcnt(0)
	v_readfirstlane_b32 s5, v9
	s_cmp_eq_u32 s5, 6
	s_cbranch_scc1 .Lsf5_done
	ds_add_rtn_u32 v9, v8, v18 offset:4
	s_waitcnt lgkmcnt(0)
	v_readfirstlane_b32 s18, v9
	s_cmp_ge_u32 s18, 64
	s_cbranch_scc1 .Lsf5_done
	s_add_i32 s18, s18, s33
	s_and_b32 s27, s18, 1
	s_lshr_b32 s19, s18, 1
	s_add_i32 s19, s19, 0x6800
	s_cmp_lt_u32 s19, 0x7000
	s_cbranch_scc0 .Lsf5_down
	s_add_i32 s20, s19, 0xffffc800
	s_lshr_b32 s21, s20, 8
	s_mul_i32 s21, s21, 37
	s_lshr_b32 s21, s21, 8
	s_mul_i32 s28, s21, 0x700
	s_sub_i32 s20, s20, s28
	s_mul_i32 s28, s21, 0x3800000
	s_add_u32 s14, s10, s28
	s_addc_u32 s15, s11, 0
	s_mul_i32 s28, s21, 0x1c00000
	s_add_u32 s28, s28, 0x7800000
	s_add_u32 s16, s86, s28
	s_addc_u32 s17, s87, 0
	s_movk_i32 s24, 0x7000
	s_movk_i32 s25, 0x800
	s_mov_b32 s26, 0x43800000
	s_lshr_b32 s22, s20, 4
	s_mul_i32 s22, s22, 0x2493
	s_lshr_b32 s22, s22, 16
	s_mul_i32 s28, s22, 0x70
	s_sub_i32 s23, s20, s28
	s_mov_b32 s29, 1
	s_branch .Lsf5_dec

; __device__ __forceinline__ void transpose_item_f8(const float* W, int N, unsigned char* WT, int ldt, int kind, int off, int item, int lane, float scale) {
;     const int nblk = N >> 6, kb = item / nblk, nb = item - kb * nblk, k0 = 128 * kb + 16 * (lane & 7), n = 64 * nb + 4 * (lane >> 3);
; __device__ __forceinline__ void moe_convert(Frame& F, int lo, int hi, int rank, int nrank) {
;     ...
;     for (int it = lo + rank; it < hi; it += nrank) {
;         int r = it; const float* W; unsigned char* WT; int N, ldt, kind, off; float f8s;
;         if (r < 14336) { const int e = r / 1792; r -= e * 1792; W = F.in[IN_WMG] + (size_t)e * 2048 * DFFE; N = DFFE; WT = F.ws + WS_WGU1 + (size_t)e * 14336 * 2048; ldt = 2048; kind = 1; off = 0; f8s = 32.f; }
;         else if ((r -= 14336) < 14336) { const int e = r / 1792; r -= e * 1792; W = F.in[IN_WMU] + (size_t)e * 2048 * DFFE; N = DFFE; WT = F.ws + WS_WGU1 + (size_t)e * 14336 * 2048; ldt = 2048; kind = 1; off = 128; f8s = 256.f; }
;         else { r -= 14336; const int e = r / 1792; r -= e * 1792; W = F.in[IN_WMD] + (size_t)e * DFFE * 2048; N = 2048; WT = F.ws + WS_WDN1 + (size_t)e * 2048 * DFFE; ldt = DFFE; kind = 0; off = 0; f8s = 64.f; }
;         transpose_item_f8(W, N, WT, ldt, kind, off, r, F.lane, f8s);
.Lsf6_loop:
	ds_read_b32 v9, v8
	s_waitcnt lgkmcnt(0)
	v_readfirstlane_b32 s5, v9
	s_cmp_eq_u32 s5, 7
	s_cbranch_scc1 .Lsf6_done
	ds_add_rtn_u32 v9, v8, v18 offset:4
	s_waitcnt lgkmcnt(0)
	v_readfirstlane_b32 s18, v9
	s_cmp_ge_u32 s18, 64
	s_cbranch_scc1 .Lsf6_done
	s_add_i32 s18, s18, s33
	s_and_b32 s27, s18, 1
	s_lshr_b32 s19, s18, 1
	s_add_i32 s19, s19, 0x6800
	s_cmp_lt_u32 s19, 0x7000
	s_cbranch_scc0 .Lsf6_down
	s_add_i32 s20, s19, 0xffffc800
	s_lshr_b32 s21, s20, 8
	s_mul_i32 s21, s21, 37
	s_lshr_b32 s21, s21, 8
	s_mul_i32 s28, s21, 0x700
	s_sub_i32 s20, s20, s28
	s_mul_i32 s28, s21, 0x3800000
	s_add_u32 s14, s10, s28
	s_addc_u32 s15, s11, 0
	s_mul_i32 s28, s21, 0x1c00000
	s_add_u32 s28, s28, 0x7800000
	s_add_u32 s16, s86, s28
	s_addc_u32 s17, s87, 0
	s_movk_i32 s24, 0x7000
	s_movk_i32 s25, 0x800
	s_mov_b32 s26, 0x43800000
	s_lshr_b32 s22, s20, 4
	s_mul_i32 s22, s22, 0x2493
	s_lshr_b32 s22, s22, 16
	s_mul_i32 s28, s22, 0x70
	s_sub_i32 s23, s20, s28
	s_mov_b32 s29, 1
	s_branch .Lsf6_dec

; __device__ __forceinline__ void moe_convert(Frame& F, int lo, int hi, int rank, int nrank) {
;     ...
;     for (int it = lo + rank; it < hi; it += nrank) {
;         int r = it; const float* W; unsigned char* WT; int N, ldt, kind, off; float f8s;
;         if (r < 14336) { const int e = r / 1792; r -= e * 1792; W = F.in[IN_WMG] + (size_t)e * 2048 * DFFE; N = DFFE; WT = F.ws + WS_WGU1 + (size_t)e * 14336 * 2048; ldt = 2048; kind = 1; off = 0; f8s = 32.f; }
;         else if ((r -= 14336) < 14336) { const int e = r / 1792; r -= e * 1792; W = F.in[IN_WMU] + (size_t)e * 2048 * DFFE; N = DFFE; WT = F.ws + WS_WGU1 + (size_t)e * 14336 * 2048; ldt = 2048; kind = 1; off = 128; f8s = 256.f; }
;         else { r -= 14336; const int e = r / 1792; r -= e * 1792; W = F.in[IN_WMD] + (size_t)e * DFFE * 2048; N = 2048; WT = F.ws + WS_WDN1 + (size_t)e * 2048 * DFFE; ldt = DFFE; kind = 0; off = 0; f8s = 64.f; }
;         transpose_item_f8(W, N, WT, ldt, kind, off, r, F.lane, f8s);
.Lsf7_loop:
	ds_read_b32 v9, v8
	s_waitcnt lgkmcnt(0)
	v_readfirstlane_b32 s5, v9
	s_cmp_eq_u32 s5, 8
	s_cbranch_scc1 .Lsf7_done
	ds_add_rtn_u32 v9, v8, v18 offset:4
	s_waitcnt lgkmcnt(0)
	v_readfirstlane_b32 s18, v9
	s_cmp_ge_u32 s18, 64
	s_cbranch_scc1 .Lsf7_done
	s_add_i32 s18, s18, s33
	s_and_b32 s27, s18, 1
	s_lshr_b32 s19, s18, 1
	s_add_i32 s19, s19, 0x6800
	s_cmp_lt_u32 s19, 0x7000
	s_cbranch_scc0 .Lsf7_down
	s_add_i32 s20, s19, 0xffffc800
	s_lshr_b32 s21, s20, 8
	s_mul_i32 s21, s21, 37
	s_lshr_b32 s21, s21, 8
	s_mul_i32 s28, s21, 0x700
	s_sub_i32 s20, s20, s28
	s_mul_i32 s28, s21, 0x3800000
	s_add_u32 s14, s10, s28
	s_addc_u32 s15, s11, 0
	s_mul_i32 s28, s21, 0x1c00000
	s_add_u32 s28, s28, 0x7800000
	s_add_u32 s16, s86, s28
	s_addc_u32 s17, s87, 0
	s_movk_i32 s24, 0x7000
	s_movk_i32 s25, 0x800
	s_mov_b32 s26, 0x43800000
	s_lshr_b32 s22, s20, 4
	s_mul_i32 s22, s22, 0x2493
	s_lshr_b32 s22, s22, 16
	s_mul_i32 s28, s22, 0x70
	s_sub_i32 s23, s20, s28
	s_mov_b32 s29, 1
	s_branch .Lsf7_dec

; __device__ __forceinline__ void moe_convert(Frame& F, int lo, int hi, int rank, int nrank) {
;     ...
;     for (int it = lo + rank; it < hi; it += nrank) {
;         int r = it; const float* W; unsigned char* WT; int N, ldt, kind, off; float f8s;
;         if (r < 14336) { const int e = r / 1792; r -= e * 1792; W = F.in[IN_WMG] + (size_t)e * 2048 * DFFE; N = DFFE; WT = F.ws + WS_WGU1 + (size_t)e * 14336 * 2048; ldt = 2048; kind = 1; off = 0; f8s = 32.f; }
;         else if ((r -= 14336) < 14336) { const int e = r / 1792; r -= e * 1792; W = F.in[IN_WMU] + (size_t)e * 2048 * DFFE; N = DFFE; WT = F.ws + WS_WGU1 + (size_t)e * 14336 * 2048; ldt = 2048; kind = 1; off = 128; f8s = 256.f; }
;         else { r -= 14336; const int e = r / 1792; r -= e * 1792; W = F.in[IN_WMD] + (size_t)e * DFFE * 2048; N = 2048; WT = F.ws + WS_WDN1 + (size_t)e * 2048 * DFFE; ldt = DFFE; kind = 0; off = 0; f8s = 64.f; }
;         transpose_item_f8(W, N, WT, ldt, kind, off, r, F.lane, f8s);
.Lsf8_loop:
	ds_read_b32 v9, v8
	s_waitcnt lgkmcnt(0)
	v_readfirstlane_b32 s5, v9
	s_cmp_eq_u32 s5, 9
	s_cbranch_scc1 .Lsf8_done
	ds_add_rtn_u32 v9, v8, v18 offset:4
	s_waitcnt lgkmcnt(0)
	v_readfirstlane_b32 s18, v9
	s_cmp_ge_u32 s18, 64
	s_cbranch_scc1 .Lsf8_done
	s_add_i32 s18, s18, s33
	s_and_b32 s27, s18, 1
	s_lshr_b32 s19, s18, 1
	s_add_i32 s19, s19, 0x6800
	s_cmp_lt_u32 s19, 0x7000
	s_cbranch_scc0 .Lsf8_down
	s_add_i32 s20, s19, 0xffffc800
	s_lshr_b32 s21, s20, 8
	s_mul_i32 s21, s21, 37
	s_lshr_b32 s21, s21, 8
	s_mul_i32 s28, s21, 0x700
	s_sub_i32 s20, s20, s28
	s_mul_i32 s28, s21, 0x3800000
	s_add_u32 s14, s10, s28
	s_addc_u32 s15, s11, 0
	s_mul_i32 s28, s21, 0x1c00000
	s_add_u32 s28, s28, 0x7800000
	s_add_u32 s16, s86, s28
	s_addc_u32 s17, s87, 0
	s_movk_i32 s24, 0x7000
	s_movk_i32 s25, 0x800
	s_mov_b32 s26, 0x43800000
	s_lshr_b32 s22, s20, 4
	s_mul_i32 s22, s22, 0x2493
	s_lshr_b32 s22, s22, 16
	s_mul_i32 s28, s22, 0x70
	s_sub_i32 s23, s20, s28
	s_mov_b32 s29, 1
	s_branch .Lsf8_dec

; __device__ __forceinline__ void moe_convert(Frame& F, int lo, int hi, int rank, int nrank) {
;     ...
;     for (int it = lo + rank; it < hi; it += nrank) {
;         int r = it; const float* W; unsigned char* WT; int N, ldt, kind, off; float f8s;
;         if (r < 14336) { const int e = r / 1792; r -= e * 1792; W = F.in[IN_WMG] + (size_t)e * 2048 * DFFE; N = DFFE; WT = F.ws + WS_WGU1 + (size_t)e * 14336 * 2048; ldt = 2048; kind = 1; off = 0; f8s = 32.f; }
;         else if ((r -= 14336) < 14336) { const int e = r / 1792; r -= e * 1792; W = F.in[IN_WMU] + (size_t)e * 2048 * DFFE; N = DFFE; WT = F.ws + WS_WGU1 + (size_t)e * 14336 * 2048; ldt = 2048; kind = 1; off = 128; f8s = 256.f; }
;         else { r -= 14336; const int e = r / 1792; r -= e * 1792; W = F.in[IN_WMD] + (size_t)e * DFFE * 2048; N = 2048; WT = F.ws + WS_WDN1 + (size_t)e * 2048 * DFFE; ldt = DFFE; kind = 0; off = 0; f8s = 64.f; }
;         transpose_item_f8(W, N, WT, ldt, kind, off, r, F.lane, f8s);
.Lsf9_loop:
	ds_read_b32 v9, v8
	s_waitcnt lgkmcnt(0)
	v_readfirstlane_b32 s5, v9
	s_cmp_eq_u32 s5, 10
	s_cbranch_scc1 .Lsf9_done
	ds_add_rtn_u32 v9, v8, v18 offset:4
	s_waitcnt lgkmcnt(0)
	v_readfirstlane_b32 s18, v9
	s_cmp_ge_u32 s18, 64
	s_cbranch_scc1 .Lsf9_done
	s_add_i32 s18, s18, s33
	s_and_b32 s27, s18, 1
	s_lshr_b32 s19, s18, 1
	s_add_i32 s19, s19, 0x6800
	s_cmp_lt_u32 s19, 0x7000
	s_cbranch_scc0 .Lsf9_down
	s_add_i32 s20, s19, 0xffffc800
	s_lshr_b32 s21, s20, 8
	s_mul_i32 s21, s21, 37
	s_lshr_b32 s21, s21, 8
	s_mul_i32 s28, s21, 0x700
	s_sub_i32 s20, s20, s28
	s_mul_i32 s28, s21, 0x3800000
	s_add_u32 s14, s10, s28
	s_addc_u32 s15, s11, 0
	s_mul_i32 s28, s21, 0x1c00000
	s_add_u32 s28, s28, 0x7800000
	s_add_u32 s16, s86, s28
	s_addc_u32 s17, s87, 0
	s_movk_i32 s24, 0x7000
	s_movk_i32 s25, 0x800
	s_mov_b32 s26, 0x43800000
	s_lshr_b32 s22, s20, 4
	s_mul_i32 s22, s22, 0x2493
	s_lshr_b32 s22, s22, 16
	s_mul_i32 s28, s22, 0x70
	s_sub_i32 s23, s20, s28
	s_mov_b32 s29, 1
	s_branch .Lsf9_dec

; __device__ __forceinline__ void moe_convert(Frame& F, int lo, int hi, int rank, int nrank) {
;     ...
;     for (int it = lo + rank; it < hi; it += nrank) {
;         int r = it; const float* W; unsigned char* WT; int N, ldt, kind, off; float f8s;
;         if (r < 14336) { const int e = r / 1792; r -= e * 1792; W = F.in[IN_WMG] + (size_t)e * 2048 * DFFE; N = DFFE; WT = F.ws + WS_WGU1 + (size_t)e * 14336 * 2048; ldt = 2048; kind = 1; off = 0; f8s = 32.f; }
;         else if ((r -= 14336) < 14336) { const int e = r / 1792; r -= e * 1792; W = F.in[IN_WMU] + (size_t)e * 2048 * DFFE; N = DFFE; WT = F.ws + WS_WGU1 + (size_t)e * 14336 * 2048; ldt = 2048; kind = 1; off = 128; f8s = 256.f; }
;         else { r -= 14336; const int e = r / 1792; r -= e * 1792; W = F.in[IN_WMD] + (size_t)e * DFFE * 2048; N = 2048; WT = F.ws + WS_WDN1 + (size_t)e * 2048 * DFFE; ldt = DFFE; kind = 0; off = 0; f8s = 64.f; }
;         transpose_item_f8(W, N, WT, ldt, kind, off, r, F.lane, f8s);
.Lsf10_loop:
	ds_read_b32 v9, v8
	s_waitcnt lgkmcnt(0)
	v_readfirstlane_b32 s5, v9
	s_cmp_eq_u32 s5, 11
	s_cbranch_scc1 .Lsf10_done
	ds_add_rtn_u32 v9, v8, v18 offset:4
	s_waitcnt lgkmcnt(0)
	v_readfirstlane_b32 s18, v9
	s_cmp_ge_u32 s18, 64
	s_cbranch_scc1 .Lsf10_done
	s_add_i32 s18, s18, s33
	s_and_b32 s27, s18, 1
	s_lshr_b32 s19, s18, 1
	s_add_i32 s19, s19, 0x6800
	s_cmp_lt_u32 s19, 0x7000
	s_cbranch_scc0 .Lsf10_down
	s_add_i32 s20, s19, 0xffffc800
	s_lshr_b32 s21, s20, 8
	s_mul_i32 s21, s21, 37
	s_lshr_b32 s21, s21, 8
	s_mul_i32 s28, s21, 0x700
	s_sub_i32 s20, s20, s28
	s_mul_i32 s28, s21, 0x3800000
	s_add_u32 s14, s10, s28
	s_addc_u32 s15, s11, 0
	s_mul_i32 s28, s21, 0x1c00000
	s_add_u32 s28, s28, 0x7800000
	s_add_u32 s16, s86, s28
	s_addc_u32 s17, s87, 0
	s_movk_i32 s24, 0x7000
	s_movk_i32 s25, 0x800
	s_mov_b32 s26, 0x43800000
	s_lshr_b32 s22, s20, 4
	s_mul_i32 s22, s22, 0x2493
	s_lshr_b32 s22, s22, 16
	s_mul_i32 s28, s22, 0x70
	s_sub_i32 s23, s20, s28
	s_mov_b32 s29, 1
	s_branch .Lsf10_dec

; __device__ __forceinline__ void moe_convert(Frame& F, int lo, int hi, int rank, int nrank) {
;     ...
;     for (int it = lo + rank; it < hi; it += nrank) {
;         int r = it; const float* W; unsigned char* WT; int N, ldt, kind, off; float f8s;
;         if (r < 14336) { const int e = r / 1792; r -= e * 1792; W = F.in[IN_WMG] + (size_t)e * 2048 * DFFE; N = DFFE; WT = F.ws + WS_WGU1 + (size_t)e * 14336 * 2048; ldt = 2048; kind = 1; off = 0; f8s = 32.f; }
;         else if ((r -= 14336) < 14336) { const int e = r / 1792; r -= e * 1792; W = F.in[IN_WMU] + (size_t)e * 2048 * DFFE; N = DFFE; WT = F.ws + WS_WGU1 + (size_t)e * 14336 * 2048; ldt = 2048; kind = 1; off = 128; f8s = 256.f; }
;         else { r -= 14336; const int e = r / 1792; r -= e * 1792; W = F.in[IN_WMD] + (size_t)e * DFFE * 2048; N = 2048; WT = F.ws + WS_WDN1 + (size_t)e * 2048 * DFFE; ldt = DFFE; kind = 0; off = 0; f8s = 64.f; }
;         transpose_item_f8(W, N, WT, ldt, kind, off, r, F.lane, f8s);
.Lsf11_loop:
	ds_read_b32 v9, v8
	s_waitcnt lgkmcnt(0)
	v_readfirstlane_b32 s5, v9
	s_cmp_eq_u32 s5, 12
	s_cbranch_scc1 .Lsf11_done
	ds_add_rtn_u32 v9, v8, v18 offset:4
	s_waitcnt lgkmcnt(0)
	v_readfirstlane_b32 s18, v9
	s_cmp_ge_u32 s18, 64
	s_cbranch_scc1 .Lsf11_done
	s_add_i32 s18, s18, s33
	s_and_b32 s27, s18, 1
	s_lshr_b32 s19, s18, 1
	s_add_i32 s19, s19, 0x6800
	s_cmp_lt_u32 s19, 0x7000
	s_cbranch_scc0 .Lsf11_down
	s_add_i32 s20, s19, 0xffffc800
	s_lshr_b32 s21, s20, 8
	s_mul_i32 s21, s21, 37
	s_lshr_b32 s21, s21, 8
	s_mul_i32 s28, s21, 0x700
	s_sub_i32 s20, s20, s28
	s_mul_i32 s28, s21, 0x3800000
	s_add_u32 s14, s10, s28
	s_addc_u32 s15, s11, 0
	s_mul_i32 s28, s21, 0x1c00000
	s_add_u32 s28, s28, 0x7800000
	s_add_u32 s16, s86, s28
	s_addc_u32 s17, s87, 0
	s_movk_i32 s24, 0x7000
	s_movk_i32 s25, 0x800
	s_mov_b32 s26, 0x43800000
	s_lshr_b32 s22, s20, 4
	s_mul_i32 s22, s22, 0x2493
	s_lshr_b32 s22, s22, 16
	s_mul_i32 s28, s22, 0x70
	s_sub_i32 s23, s20, s28
	s_mov_b32 s29, 1
	s_branch .Lsf11_dec

; __device__ __forceinline__ void moe_convert(Frame& F, int lo, int hi, int rank, int nrank) {
;     ...
;     for (int it = lo + rank; it < hi; it += nrank) {
;         int r = it; const float* W; unsigned char* WT; int N, ldt, kind, off; float f8s;
;         if (r < 14336) { const int e = r / 1792; r -= e * 1792; W = F.in[IN_WMG] + (size_t)e * 2048 * DFFE; N = DFFE; WT = F.ws + WS_WGU1 + (size_t)e * 14336 * 2048; ldt = 2048; kind = 1; off = 0; f8s = 32.f; }
;         else if ((r -= 14336) < 14336) { const int e = r / 1792; r -= e * 1792; W = F.in[IN_WMU] + (size_t)e * 2048 * DFFE; N = DFFE; WT = F.ws + WS_WGU1 + (size_t)e * 14336 * 2048; ldt = 2048; kind = 1; off = 128; f8s = 256.f; }
;         else { r -= 14336; const int e = r / 1792; r -= e * 1792; W = F.in[IN_WMD] + (size_t)e * DFFE * 2048; N = 2048; WT = F.ws + WS_WDN1 + (size_t)e * 2048 * DFFE; ldt = DFFE; kind = 0; off = 0; f8s = 64.f; }
;         transpose_item_f8(W, N, WT, ldt, kind, off, r, F.lane, f8s);
.Lsf12_loop:
	ds_read_b32 v9, v8
	s_waitcnt lgkmcnt(0)
	v_readfirstlane_b32 s5, v9
	s_cmp_eq_u32 s5, 13
	s_cbranch_scc1 .Lsf12_done
	ds_add_rtn_u32 v9, v8, v18 offset:4
	s_waitcnt lgkmcnt(0)
	v_readfirstlane_b32 s18, v9
	s_cmp_ge_u32 s18, 64
	s_cbranch_scc1 .Lsf12_done
	s_add_i32 s18, s18, s33
	s_and_b32 s27, s18, 1
	s_lshr_b32 s19, s18, 1
	s_add_i32 s19, s19, 0x6800
	s_cmp_lt_u32 s19, 0x7000
	s_cbranch_scc0 .Lsf12_down
	s_add_i32 s20, s19, 0xffffc800
	s_lshr_b32 s21, s20, 8
	s_mul_i32 s21, s21, 37
	s_lshr_b32 s21, s21, 8
	s_mul_i32 s28, s21, 0x700
	s_sub_i32 s20, s20, s28
	s_mul_i32 s28, s21, 0x3800000
	s_add_u32 s14, s10, s28
	s_addc_u32 s15, s11, 0
	s_mul_i32 s28, s21, 0x1c00000
	s_add_u32 s28, s28, 0x7800000
	s_add_u32 s16, s86, s28
	s_addc_u32 s17, s87, 0
	s_movk_i32 s24, 0x7000
	s_movk_i32 s25, 0x800
	s_mov_b32 s26, 0x43800000
	s_lshr_b32 s22, s20, 4
	s_mul_i32 s22, s22, 0x2493
	s_lshr_b32 s22, s22, 16
	s_mul_i32 s28, s22, 0x70
	s_sub_i32 s23, s20, s28
	s_mov_b32 s29, 1
	s_branch .Lsf12_dec

; __device__ __forceinline__ void moe_convert(Frame& F, int lo, int hi, int rank, int nrank) {
;     ...
;     for (int it = lo + rank; it < hi; it += nrank) {
;         int r = it; const float* W; unsigned char* WT; int N, ldt, kind, off; float f8s;
;         if (r < 14336) { const int e = r / 1792; r -= e * 1792; W = F.in[IN_WMG] + (size_t)e * 2048 * DFFE; N = DFFE; WT = F.ws + WS_WGU1 + (size_t)e * 14336 * 2048; ldt = 2048; kind = 1; off = 0; f8s = 32.f; }
;         else if ((r -= 14336) < 14336) { const int e = r / 1792; r -= e * 1792; W = F.in[IN_WMU] + (size_t)e * 2048 * DFFE; N = DFFE; WT = F.ws + WS_WGU1 + (size_t)e * 14336 * 2048; ldt = 2048; kind = 1; off = 128; f8s = 256.f; }
;         else { r -= 14336; const int e = r / 1792; r -= e * 1792; W = F.in[IN_WMD] + (size_t)e * DFFE * 2048; N = 2048; WT = F.ws + WS_WDN1 + (size_t)e * 2048 * DFFE; ldt = DFFE; kind = 0; off = 0; f8s = 64.f; }
;         transpose_item_f8(W, N, WT, ldt, kind, off, r, F.lane, f8s);
.Lsf13_loop:
	ds_read_b32 v9, v8
	s_waitcnt lgkmcnt(0)
	v_readfirstlane_b32 s5, v9
	s_cmp_eq_u32 s5, 14
	s_cbranch_scc1 .Lsf13_done
	ds_add_rtn_u32 v9, v8, v18 offset:4
	s_waitcnt lgkmcnt(0)
	v_readfirstlane_b32 s18, v9
	s_cmp_ge_u32 s18, 64
	s_cbranch_scc1 .Lsf13_done
	s_add_i32 s18, s18, s33
	s_and_b32 s27, s18, 1
	s_lshr_b32 s19, s18, 1
	s_add_i32 s19, s19, 0x6800
	s_cmp_lt_u32 s19, 0x7000
	s_cbranch_scc0 .Lsf13_down
	s_add_i32 s20, s19, 0xffffc800
	s_lshr_b32 s21, s20, 8
	s_mul_i32 s21, s21, 37
	s_lshr_b32 s21, s21, 8
	s_mul_i32 s28, s21, 0x700
	s_sub_i32 s20, s20, s28
	s_mul_i32 s28, s21, 0x3800000
	s_add_u32 s14, s10, s28
	s_addc_u32 s15, s11, 0
	s_mul_i32 s28, s21, 0x1c00000
	s_add_u32 s28, s28, 0x7800000
	s_add_u32 s16, s86, s28
	s_addc_u32 s17, s87, 0
	s_movk_i32 s24, 0x7000
	s_movk_i32 s25, 0x800
	s_mov_b32 s26, 0x43800000
	s_lshr_b32 s22, s20, 4
	s_mul_i32 s22, s22, 0x2493
	s_lshr_b32 s22, s22, 16
	s_mul_i32 s28, s22, 0x70
	s_sub_i32 s23, s20, s28
	s_mov_b32 s29, 1
	s_branch .Lsf13_dec

; __device__ __forceinline__ void moe_convert(Frame& F, int lo, int hi, int rank, int nrank) {
;     ...
;     for (int it = lo + rank; it < hi; it += nrank) {
;         int r = it; const float* W; unsigned char* WT; int N, ldt, kind, off; float f8s;
;         if (r < 14336) { const int e = r / 1792; r -= e * 1792; W = F.in[IN_WMG] + (size_t)e * 2048 * DFFE; N = DFFE; WT = F.ws + WS_WGU1 + (size_t)e * 14336 * 2048; ldt = 2048; kind = 1; off = 0; f8s = 32.f; }
;         else if ((r -= 14336) < 14336) { const int e = r / 1792; r -= e * 1792; W = F.in[IN_WMU] + (size_t)e * 2048 * DFFE; N = DFFE; WT = F.ws + WS_WGU1 + (size_t)e * 14336 * 2048; ldt = 2048; kind = 1; off = 128; f8s = 256.f; }
;         else { r -= 14336; const int e = r / 1792; r -= e * 1792; W = F.in[IN_WMD] + (size_t)e * DFFE * 2048; N = 2048; WT = F.ws + WS_WDN1 + (size_t)e * 2048 * DFFE; ldt = DFFE; kind = 0; off = 0; f8s = 64.f; }
;         transpose_item_f8(W, N, WT, ldt, kind, off, r, F.lane, f8s);
.Lsf14_loop:
	ds_read_b32 v9, v8
	s_waitcnt lgkmcnt(0)
	v_readfirstlane_b32 s5, v9
	s_cmp_eq_u32 s5, 15
	s_cbranch_scc1 .Lsf14_done
	ds_add_rtn_u32 v9, v8, v18 offset:4
	s_waitcnt lgkmcnt(0)
	v_readfirstlane_b32 s18, v9
	s_cmp_ge_u32 s18, 64
	s_cbranch_scc1 .Lsf14_done
	s_add_i32 s18, s18, s33
	s_and_b32 s27, s18, 1
	s_lshr_b32 s19, s18, 1
	s_add_i32 s19, s19, 0x6800
	s_cmp_lt_u32 s19, 0x7000
	s_cbranch_scc0 .Lsf14_down
	s_add_i32 s20, s19, 0xffffc800
	s_lshr_b32 s21, s20, 8
	s_mul_i32 s21, s21, 37
	s_lshr_b32 s21, s21, 8
	s_mul_i32 s28, s21, 0x700
	s_sub_i32 s20, s20, s28
	s_mul_i32 s28, s21, 0x3800000
	s_add_u32 s14, s10, s28
	s_addc_u32 s15, s11, 0
	s_mul_i32 s28, s21, 0x1c00000
	s_add_u32 s28, s28, 0x7800000
	s_add_u32 s16, s86, s28
	s_addc_u32 s17, s87, 0
	s_movk_i32 s24, 0x7000
	s_movk_i32 s25, 0x800
	s_mov_b32 s26, 0x43800000
	s_lshr_b32 s22, s20, 4
	s_mul_i32 s22, s22, 0x2493
	s_lshr_b32 s22, s22, 16
	s_mul_i32 s28, s22, 0x70
	s_sub_i32 s23, s20, s28
	s_mov_b32 s29, 1
	s_branch .Lsf14_dec

; __device__ __forceinline__ void moe_convert(Frame& F, int lo, int hi, int rank, int nrank) {
;     if (MOE_DMA) { moe_convert_dma(F, lo, hi, rank, nrank); return; }
;     for (int it = lo + rank; it < hi; it += nrank) {
;         int r = it; const float* W; unsigned char* WT; int N, ldt, kind, off; float f8s;
;         if (r < 14336) { const int e = r / 1792; r -= e * 1792; W = F.in[IN_WMG] + (size_t)e * 2048 * DFFE; N = DFFE; WT = F.ws + WS_WGU1 + (size_t)e * 14336 * 2048; ldt = 2048; kind = 1; off = 0; f8s = 32.f; }
;         else if ((r -= 14336) < 14336) { const int e = r / 1792; r -= e * 1792; W = F.in[IN_WMU] + (size_t)e * 2048 * DFFE; N = DFFE; WT = F.ws + WS_WGU1 + (size_t)e * 14336 * 2048; ldt = 2048; kind = 1; off = 128; f8s = 256.f; }
;         else { r -= 14336; const int e = r / 1792; r -= e * 1792; W = F.in[IN_WMD] + (size_t)e * DFFE * 2048; N = 2048; WT = F.ws + WS_WDN1 + (size_t)e * 2048 * DFFE; ldt = DFFE; kind = 0; off = 0; f8s = 64.f; }
;         transpose_item_f8(W, N, WT, ldt, kind, off, r, F.lane, f8s);
.Lsf15_notw0:
	s_cmp_gt_u32 s4, 4
	s_cbranch_scc1 .Lsf15_skip
	v_mov_b32_e32 v8, 0x20020
	ds_read_b32 v9, v8 offset:4
	v_mbcnt_lo_u32_b32 v2, -1, 0
	v_mbcnt_hi_u32_b32 v2, -1, v2
	s_waitcnt lgkmcnt(0)
	v_readfirstlane_b32 s5, v9
	s_cmp_ge_u32 s5, 64
	s_cbranch_scc1 .Lsf15_skip
	s_add_i32 s5, s4, -1
	s_lshl_b32 s5, s5, 14
	v_lshl_add_u32 v7, v2, 4, s5
	ds_write_b128 v7, v[160:163] offset:0
	ds_write_b128 v7, v[164:167] offset:1024
	ds_write_b128 v7, v[168:171] offset:2048
	ds_write_b128 v7, v[172:175] offset:3072
	ds_write_b128 v7, v[176:179] offset:4096
	ds_write_b128 v7, v[180:183] offset:5120
	ds_write_b128 v7, v[184:187] offset:6144
	ds_write_b128 v7, v[188:191] offset:7168
	ds_write_b128 v7, v[192:195] offset:8192
	ds_write_b128 v7, v[196:199] offset:9216
	ds_write_b128 v7, v[200:203] offset:10240
	ds_write_b128 v7, v[204:207] offset:11264
	ds_write_b128 v7, v[208:211] offset:12288
	ds_write_b128 v7, v[212:215] offset:13312
	ds_write_b128 v7, v[216:219] offset:14336
	ds_write_b128 v7, v[220:223] offset:15360
	v_readlane_b32 s6, v247, 0
	v_readlane_b32 s7, v247, 1
	s_load_dwordx2 s[10:11], s[6:7], 0xc0
	s_load_dwordx2 s[12:13], s[6:7], 0xc8
	v_readlane_b32 s33, v247, 6
	v_mov_b32_e32 v3, 0x43e00000
	v_cmp_eq_u32_e32 vcc, 0, v2
	s_mul_i32 s33, s33, 64
	s_nop 1
	v_cndmask_b32_e64 v18, 0, 1, vcc
	s_waitcnt lgkmcnt(0)
.Lsf15_loop:
	ds_add_rtn_u32 v9, v8, v18 offset:4
	s_waitcnt lgkmcnt(0)
	v_readfirstlane_b32 s18, v9
	s_cmp_ge_u32 s18, 64
	s_cbranch_scc1 .Lsf15_done
	s_add_i32 s18, s18, s33
	s_and_b32 s27, s18, 1
	s_lshr_b32 s19, s18, 1
	s_add_i32 s19, s19, 0x6800
	s_cmp_lt_u32 s19, 0x7000
	s_cbranch_scc0 .Lsf15_down
	s_add_i32 s20, s19, 0xffffc800
	s_lshr_b32 s21, s20, 8
	s_mul_i32 s21, s21, 37
	s_lshr_b32 s21, s21, 8
	s_mul_i32 s28, s21, 0x700
	s_sub_i32 s20, s20, s28
	s_mul_i32 s28, s21, 0x3800000
	s_add_u32 s14, s10, s28
	s_addc_u32 s15, s11, 0
	s_mul_i32 s28, s21, 0x1c00000
	s_add_u32 s28, s28, 0x7800000
	s_add_u32 s16, s86, s28
	s_addc_u32 s17, s87, 0
	s_movk_i32 s24, 0x7000
	s_movk_i32 s25, 0x800
	s_mov_b32 s26, 0x43800000
	s_lshr_b32 s22, s20, 4
	s_mul_i32 s22, s22, 0x2493
	s_lshr_b32 s22, s22, 16
	s_mul_i32 s28, s22, 0x70
	s_sub_i32 s23, s20, s28
	s_mov_b32 s29, 1
	s_branch .Lsf15_dec
